# ssd_out inter-chunk product: the 32 carried-state fragment loads issued in consumption order through a pool of 18 free quads (18 up front, then one per MFMA), counted vmcnt; the compiler's schedule ex
# baseline (speedup 1.0000x reference)
.LBB0_552:
	s_andn2_saveexec_b64 s[40:41], s[40:41]
	v_lshl_or_b32 v0, s87, 8, v134
	v_mov_b32_e32 v136, 0x2000
	s_or_b64 exec, exec, s[40:41]
	v_lshlrev_b64 v[94:95], 2, v[0:1]
	v_lshl_add_u64 v[86:87], s[74:75], 0, v[94:95]
	v_add_co_u32_e32 v80, vcc, 0x2000, v86
	s_mov_b64 s[40:41], 0x2000
	s_nop 0
	v_addc_co_u32_e32 v81, vcc, 0, v87, vcc
	v_lshl_add_u64 v[78:79], v[86:87], 0, s[40:41]
	s_mov_b64 s[40:41], 0x4000
	v_add_co_u32_e32 v84, vcc, 0x4000, v86
	v_lshl_add_u64 v[82:83], v[86:87], 0, s[40:41]
	s_nop 0
	v_addc_co_u32_e32 v85, vcc, 0, v87, vcc
	s_mov_b64 s[40:41], 0x6000
	global_load_dwordx4 v[90:93], v[86:87], off offset:16
	global_load_dwordx4 v[110:113], v[86:87], off
	v_lshl_add_u64 v[88:89], v[86:87], 0, s[40:41]
	v_add_co_u32_e32 v86, vcc, 0x6000, v86
	v_lshl_add_u64 v[114:115], s[76:77], 0, v[94:95]
	s_nop 0
	v_addc_co_u32_e32 v87, vcc, 0, v87, vcc
	global_load_dwordx4 v[98:101], v[80:81], off
	s_nop 0
	global_load_dwordx4 v[78:81], v[78:79], off offset:16
	s_nop 0
	global_load_dwordx4 v[102:105], v[84:85], off
	s_nop 0
	global_load_dwordx4 v[82:85], v[82:83], off offset:16
	s_nop 0
	global_load_dwordx4 v[106:109], v[86:87], off
	s_nop 0
	global_load_dwordx4 v[86:89], v[88:89], off offset:16
	s_nop 0
	global_load_dwordx4 v[94:97], v[114:115], off offset:16
	s_nop 0
	global_load_dwordx4 v[114:117], v[114:115], off
	v_and_b32_e32 v0, 24, v118
	v_add_lshl_u32 v0, v135, v0, 6
	v_mov_b32_e32 v121, 1.0
	v_add_u32_e32 v0, 0, v0
	v_mov_b32_e32 v120, 1.0
	s_and_saveexec_b64 s[40:41], s[38:39]
	ds_read_b32 v120, v0
	s_or_b64 exec, exec, s[40:41]
	s_and_saveexec_b64 s[40:41], s[38:39]
	ds_read_b32 v121, v0 offset:4
	s_or_b64 exec, exec, s[40:41]
	v_mov_b32_e32 v125, 1.0
	v_mov_b32_e32 v124, 1.0
	s_and_saveexec_b64 s[40:41], s[38:39]
	ds_read_b32 v124, v0 offset:8
	s_or_b64 exec, exec, s[40:41]
	s_and_saveexec_b64 s[40:41], s[38:39]
	ds_read_b32 v125, v0 offset:12
	s_or_b64 exec, exec, s[40:41]
	v_mov_b32_e32 v119, 1.0
	v_mov_b32_e32 v118, 1.0
	s_and_saveexec_b64 s[40:41], s[38:39]
	ds_read_b32 v118, v0 offset:16
	s_or_b64 exec, exec, s[40:41]
	s_and_saveexec_b64 s[40:41], s[38:39]
	ds_read_b32 v119, v0 offset:20
	s_or_b64 exec, exec, s[40:41]
	v_mov_b32_e32 v127, 1.0
	v_mov_b32_e32 v126, 1.0
	s_and_saveexec_b64 s[40:41], s[38:39]
	ds_read_b32 v126, v0 offset:24
	s_or_b64 exec, exec, s[40:41]
	s_and_saveexec_b64 s[40:41], s[38:39]
	ds_read_b32 v127, v0 offset:28
	s_or_b64 exec, exec, s[40:41]
	v_mov_b32_e32 v129, 1.0
	v_mov_b32_e32 v128, 1.0
	s_and_saveexec_b64 s[40:41], s[38:39]
	ds_read_b32 v128, v0 offset:32
	s_or_b64 exec, exec, s[40:41]
	s_and_saveexec_b64 s[40:41], s[38:39]
	ds_read_b32 v129, v0 offset:36
	s_or_b64 exec, exec, s[40:41]
	v_mov_b32_e32 v123, 1.0
	v_mov_b32_e32 v122, 1.0
	s_and_saveexec_b64 s[40:41], s[38:39]
	ds_read_b32 v122, v0 offset:40
	s_or_b64 exec, exec, s[40:41]
	s_and_saveexec_b64 s[40:41], s[38:39]
	ds_read_b32 v123, v0 offset:44
	s_or_b64 exec, exec, s[40:41]
	v_mov_b32_e32 v131, 1.0
	v_mov_b32_e32 v130, 1.0
	s_and_saveexec_b64 s[40:41], s[38:39]
	ds_read_b32 v130, v0 offset:48
	s_or_b64 exec, exec, s[40:41]
	s_and_saveexec_b64 s[40:41], s[38:39]
	ds_read_b32 v131, v0 offset:52
	s_or_b64 exec, exec, s[40:41]
	v_mov_b32_e32 v133, 1.0
	v_mov_b32_e32 v132, 1.0
	s_and_saveexec_b64 s[40:41], s[38:39]
	ds_read_b32 v132, v0 offset:56
	s_or_b64 exec, exec, s[40:41]
	s_and_saveexec_b64 s[40:41], s[38:39]
	ds_read_b32 v133, v0 offset:60
	s_or_b64 exec, exec, s[40:41]
	v_lshlrev_b32_e32 v164, 16, v2
	v_lshlrev_b32_e32 v165, 16, v14
	v_lshlrev_b32_e32 v167, 16, v10
	v_lshlrev_b32_e32 v166, 16, v6
	s_waitcnt vmcnt(0)
	v_pk_fma_f32 v[168:169], v[110:111], v[166:167], v[114:115] op_sel_hi:[0,1,0]
	v_pk_mov_b32 v[166:167], v[166:167], v[164:165] op_sel:[1,0]
	v_lshlrev_b32_e32 v163, 16, v22
	v_lshlrev_b32_e32 v162, 16, v18
	v_pk_fma_f32 v[166:167], v[98:99], v[166:167], v[168:169] op_sel_hi:[0,1,1]
	v_pk_mov_b32 v[170:171], v[164:165], v[162:163] op_sel:[1,0]
	v_pk_fma_f32 v[166:167], v[102:103], v[164:165], v[166:167] op_sel_hi:[0,1,1]
	v_pk_fma_f32 v[166:167], v[106:107], v[170:171], v[166:167] op_sel_hi:[0,1,1]
	v_mul_f32_e32 v137, 0xbfb8aa3b, v166
	v_exp_f32_e32 v137, v137
	v_mul_f32_e32 v142, 0xbfb8aa3b, v167
	v_exp_f32_e32 v142, v142
	v_pk_fma_f32 v[164:165], v[110:111], v[164:165], v[114:115] op_sel_hi:[0,1,0]
	v_lshlrev_b32_e32 v159, 16, v30
	v_lshlrev_b32_e32 v158, 16, v26
	v_pk_fma_f32 v[164:165], v[98:99], v[170:171], v[164:165] op_sel_hi:[0,1,1]
	v_pk_mov_b32 v[172:173], v[162:163], v[158:159] op_sel:[1,0]
	v_pk_fma_f32 v[164:165], v[102:103], v[162:163], v[164:165] op_sel_hi:[0,1,1]
	v_add_f32_e32 v137, 1.0, v137
	v_pk_fma_f32 v[164:165], v[106:107], v[172:173], v[164:165] op_sel_hi:[0,1,1]
	v_rcp_f32_e32 v168, v137
	v_add_f32_e32 v137, 1.0, v142
	v_mul_f32_e32 v142, 0xbfb8aa3b, v164
	v_mul_f32_e32 v169, 0xbfb8aa3b, v165
	v_exp_f32_e32 v142, v142
	v_exp_f32_e32 v171, v169
	v_rcp_f32_e32 v169, v137
	v_pk_fma_f32 v[162:163], v[110:111], v[162:163], v[114:115] op_sel_hi:[0,1,0]
	v_lshlrev_b32_e32 v155, 16, v38
	v_lshlrev_b32_e32 v154, 16, v34
	v_pk_fma_f32 v[162:163], v[98:99], v[172:173], v[162:163] op_sel_hi:[0,1,1]
	v_pk_fma_f32 v[160:161], v[110:111], v[158:159], v[114:115] op_sel_hi:[0,1,0]
	v_add_f32_e32 v137, 1.0, v142
	v_pk_mul_f32 v[166:167], v[166:167], v[168:169]
	v_pk_mov_b32 v[168:169], v[158:159], v[154:155] op_sel:[1,0]
	v_pk_fma_f32 v[158:159], v[102:103], v[158:159], v[162:163] op_sel_hi:[0,1,1]
	v_rcp_f32_e32 v170, v137
	v_add_f32_e32 v137, 1.0, v171
	v_pk_fma_f32 v[158:159], v[106:107], v[168:169], v[158:159] op_sel_hi:[0,1,1]
	v_rcp_f32_e32 v171, v137
	v_mul_f32_e32 v137, 0xbfb8aa3b, v158
	v_exp_f32_e32 v137, v137
	v_mul_f32_e32 v142, 0xbfb8aa3b, v159
	v_exp_f32_e32 v142, v142
	v_lshlrev_b32_e32 v151, 16, v46
	v_lshlrev_b32_e32 v150, 16, v42
	v_pk_fma_f32 v[160:161], v[98:99], v[168:169], v[160:161] op_sel_hi:[0,1,1]
	v_pk_fma_f32 v[156:157], v[110:111], v[154:155], v[114:115] op_sel_hi:[0,1,0]
	v_pk_mul_f32 v[164:165], v[164:165], v[170:171]
	v_add_f32_e32 v137, 1.0, v137
	v_pk_mov_b32 v[170:171], v[154:155], v[150:151] op_sel:[1,0]
	v_pk_fma_f32 v[154:155], v[102:103], v[154:155], v[160:161] op_sel_hi:[0,1,1]
	s_waitcnt lgkmcnt(0)
	v_pk_mul_f32 v[162:163], v[164:165], v[124:125]
	v_rcp_f32_e32 v164, v137
	v_add_f32_e32 v137, 1.0, v142
	v_pk_fma_f32 v[154:155], v[106:107], v[170:171], v[154:155] op_sel_hi:[0,1,1]
	v_rcp_f32_e32 v165, v137
	v_mul_f32_e32 v137, 0xbfb8aa3b, v154
	v_exp_f32_e32 v137, v137
	v_mul_f32_e32 v142, 0xbfb8aa3b, v155
	v_exp_f32_e32 v142, v142
	v_lshlrev_b32_e32 v147, 16, v54
	v_lshlrev_b32_e32 v146, 16, v50
	v_pk_fma_f32 v[156:157], v[98:99], v[170:171], v[156:157] op_sel_hi:[0,1,1]
	v_pk_fma_f32 v[152:153], v[110:111], v[150:151], v[114:115] op_sel_hi:[0,1,0]
	v_pk_mul_f32 v[158:159], v[158:159], v[164:165]
	v_pk_mov_b32 v[164:165], v[150:151], v[146:147] op_sel:[1,0]
	v_pk_fma_f32 v[150:151], v[102:103], v[150:151], v[156:157] op_sel_hi:[0,1,1]
	v_add_f32_e32 v137, 1.0, v137
	v_pk_fma_f32 v[150:151], v[106:107], v[164:165], v[150:151] op_sel_hi:[0,1,1]
	v_rcp_f32_e32 v160, v137
	v_add_f32_e32 v137, 1.0, v142
	v_mul_f32_e32 v142, 0xbfb8aa3b, v150
	v_exp_f32_e32 v142, v142
	v_mul_f32_e32 v156, 0xbfb8aa3b, v151
	v_exp_f32_e32 v157, v156
	v_rcp_f32_e32 v161, v137
	v_add_f32_e32 v137, 1.0, v142
	v_rcp_f32_e32 v156, v137
	v_add_f32_e32 v137, 1.0, v157
	v_rcp_f32_e32 v157, v137
	v_lshlrev_b32_e32 v138, 16, v58
	v_lshlrev_b32_e32 v139, 16, v66
	v_pk_fma_f32 v[152:153], v[98:99], v[164:165], v[152:153] op_sel_hi:[0,1,1]
	v_pk_fma_f32 v[148:149], v[110:111], v[146:147], v[114:115] op_sel_hi:[0,1,0]
	v_pk_mul_f32 v[150:151], v[150:151], v[156:157]
	v_pk_mov_b32 v[156:157], v[146:147], v[138:139] op_sel:[1,0]
	v_pk_fma_f32 v[146:147], v[102:103], v[146:147], v[152:153] op_sel_hi:[0,1,1]
	v_pk_fma_f32 v[146:147], v[106:107], v[156:157], v[146:147] op_sel_hi:[0,1,1]
	v_mul_f32_e32 v137, 0xbfb8aa3b, v146
	v_exp_f32_e32 v137, v137
	v_mul_f32_e32 v142, 0xbfb8aa3b, v147
	v_exp_f32_e32 v142, v142
	v_pk_fma_f32 v[148:149], v[98:99], v[156:157], v[148:149] op_sel_hi:[0,1,1]
	v_lshlrev_b32_e32 v141, 16, v62
	v_mov_b32_e32 v140, v139
	v_add_f32_e32 v137, 1.0, v137
	v_pk_fma_f32 v[148:149], v[102:103], v[138:139], v[148:149] op_sel_hi:[0,1,1]
	v_rcp_f32_e32 v152, v137
	v_add_f32_e32 v137, 1.0, v142
	v_pk_fma_f32 v[148:149], v[106:107], v[140:141], v[148:149] op_sel_hi:[0,1,1]
	v_rcp_f32_e32 v153, v137
	v_mul_f32_e32 v137, 0xbfb8aa3b, v148
	v_exp_f32_e32 v137, v137
	v_mul_f32_e32 v142, 0xbfb8aa3b, v149
	v_exp_f32_e32 v142, v142
	v_pk_fma_f32 v[138:139], v[110:111], v[138:139], v[114:115] op_sel_hi:[0,1,0]
	v_lshlrev_b32_e32 v145, 16, v70
	v_mov_b32_e32 v144, v141
	v_add_f32_e32 v137, 1.0, v137
	v_pk_fma_f32 v[138:139], v[98:99], v[140:141], v[138:139] op_sel_hi:[0,1,1]
	v_lshlrev_b32_e32 v143, 16, v74
	v_pk_mul_f32 v[146:147], v[146:147], v[152:153]
	v_rcp_f32_e32 v152, v137
	v_add_f32_e32 v137, 1.0, v142
	v_mov_b32_e32 v142, v145
	v_pk_fma_f32 v[138:139], v[102:103], v[144:145], v[138:139] op_sel_hi:[0,1,1]
	v_pk_fma_f32 v[138:139], v[106:107], v[142:143], v[138:139] op_sel_hi:[0,1,1]
	v_mul_f32_e32 v140, 0xbfb8aa3b, v138
	v_exp_f32_e32 v140, v140
	v_mul_f32_e32 v141, 0xbfb8aa3b, v139
	v_exp_f32_e32 v141, v141
	v_rcp_f32_e32 v153, v137
	v_add_f32_e32 v137, 1.0, v140
	v_rcp_f32_e32 v140, v137
	v_add_f32_e32 v137, 1.0, v141
	v_rcp_f32_e32 v141, v137
	v_pk_mul_f32 v[166:167], v[166:167], v[120:121]
	v_pk_mul_f32 v[142:143], v[148:149], v[152:153]
	v_and_b32_e32 v165, 0xffff0000, v14
	v_pk_mul_f32 v[138:139], v[138:139], v[140:141]
	v_and_b32_e32 v164, 0xffff0000, v2
	v_pk_mul_f32 v[148:149], v[138:139], v[132:133]
	v_cvt_pk_bf16_f32 v138, v166, v167
	v_and_b32_e32 v167, 0xffff0000, v10
	v_and_b32_e32 v166, 0xffff0000, v6
	v_pk_fma_f32 v[168:169], v[110:111], v[166:167], v[114:115] op_sel:[1,0,1]
	v_pk_mov_b32 v[166:167], v[166:167], v[164:165] op_sel:[1,0]
	v_cvt_pk_bf16_f32 v139, v162, v163
	v_and_b32_e32 v163, 0xffff0000, v22
	v_and_b32_e32 v162, 0xffff0000, v18
	v_pk_fma_f32 v[166:167], v[98:99], v[166:167], v[168:169] op_sel:[1,0,0]
	v_pk_mov_b32 v[170:171], v[164:165], v[162:163] op_sel:[1,0]
	v_pk_fma_f32 v[166:167], v[102:103], v[164:165], v[166:167] op_sel:[1,0,0]
	v_pk_mul_f32 v[158:159], v[158:159], v[118:119]
	v_pk_fma_f32 v[166:167], v[106:107], v[170:171], v[166:167] op_sel:[1,0,0]
	v_pk_fma_f32 v[164:165], v[110:111], v[164:165], v[114:115] op_sel:[1,0,1]
	v_mul_f32_e32 v2, 0xbfb8aa3b, v166
	v_exp_f32_e32 v2, v2
	v_mul_f32_e32 v6, 0xbfb8aa3b, v167
	v_exp_f32_e32 v6, v6
	v_cvt_pk_bf16_f32 v140, v158, v159
	v_and_b32_e32 v159, 0xffff0000, v30
	v_and_b32_e32 v158, 0xffff0000, v26
	v_pk_fma_f32 v[164:165], v[98:99], v[170:171], v[164:165] op_sel:[1,0,0]
	v_pk_mov_b32 v[172:173], v[162:163], v[158:159] op_sel:[1,0]
	v_pk_fma_f32 v[164:165], v[102:103], v[162:163], v[164:165] op_sel:[1,0,0]
	v_add_f32_e32 v2, 1.0, v2
	v_pk_fma_f32 v[164:165], v[106:107], v[172:173], v[164:165] op_sel:[1,0,0]
	v_rcp_f32_e32 v168, v2
	v_add_f32_e32 v2, 1.0, v6
	v_mul_f32_e32 v6, 0xbfb8aa3b, v164
	v_exp_f32_e32 v6, v6
	v_mul_f32_e32 v10, 0xbfb8aa3b, v165
	v_rcp_f32_e32 v169, v2
	v_pk_mul_f32 v[154:155], v[154:155], v[160:161]
	v_exp_f32_e32 v10, v10
	v_pk_mul_f32 v[154:155], v[154:155], v[126:127]
	v_pk_fma_f32 v[162:163], v[110:111], v[162:163], v[114:115] op_sel:[1,0,1]
	v_cvt_pk_bf16_f32 v141, v154, v155
	v_and_b32_e32 v155, 0xffff0000, v38
	v_and_b32_e32 v154, 0xffff0000, v34
	v_pk_fma_f32 v[162:163], v[98:99], v[172:173], v[162:163] op_sel:[1,0,0]
	v_pk_fma_f32 v[160:161], v[110:111], v[158:159], v[114:115] op_sel:[1,0,1]
	v_add_f32_e32 v2, 1.0, v6
	v_pk_mul_f32 v[166:167], v[166:167], v[168:169]
	v_pk_mov_b32 v[168:169], v[158:159], v[154:155] op_sel:[1,0]
	v_pk_fma_f32 v[158:159], v[102:103], v[158:159], v[162:163] op_sel:[1,0,0]
	v_rcp_f32_e32 v170, v2
	v_add_f32_e32 v2, 1.0, v10
	v_pk_fma_f32 v[158:159], v[106:107], v[168:169], v[158:159] op_sel:[1,0,0]
	v_rcp_f32_e32 v171, v2
	v_mul_f32_e32 v2, 0xbfb8aa3b, v158
	v_exp_f32_e32 v2, v2
	v_mul_f32_e32 v6, 0xbfb8aa3b, v159
	v_exp_f32_e32 v6, v6
	v_pk_mul_f32 v[150:151], v[150:151], v[128:129]
	v_pk_mul_f32 v[144:145], v[146:147], v[122:123]
	v_pk_mul_f32 v[146:147], v[142:143], v[130:131]
	v_cvt_pk_bf16_f32 v142, v150, v151
	v_and_b32_e32 v151, 0xffff0000, v46
	v_and_b32_e32 v150, 0xffff0000, v42
	v_pk_fma_f32 v[160:161], v[98:99], v[168:169], v[160:161] op_sel:[1,0,0]
	v_cvt_pk_bf16_f32 v143, v144, v145
	v_cvt_pk_bf16_f32 v144, v146, v147
	v_lshlrev_b32_e32 v146, 2, v134
	v_pk_fma_f32 v[156:157], v[110:111], v[154:155], v[114:115] op_sel:[1,0,1]
	v_pk_mul_f32 v[164:165], v[164:165], v[170:171]
	v_add_f32_e32 v2, 1.0, v2
	v_pk_mov_b32 v[170:171], v[154:155], v[150:151] op_sel:[1,0]
	v_pk_fma_f32 v[154:155], v[102:103], v[154:155], v[160:161] op_sel:[1,0,0]
	v_add_u32_e32 v0, 0, v136
	v_lshlrev_b32_e32 v136, 1, v135
	v_and_b32_e32 v146, 12, v146
	v_bfe_u32 v147, v134, 2, 2
	v_pk_mul_f32 v[162:163], v[164:165], v[124:125]
	v_rcp_f32_e32 v164, v2
	v_add_f32_e32 v2, 1.0, v6
	v_pk_fma_f32 v[154:155], v[106:107], v[170:171], v[154:155] op_sel:[1,0,0]
	v_cvt_pk_bf16_f32 v145, v148, v149
	v_bitop3_b32 v148, v146, v136, v147 bitop3:0x36
	v_rcp_f32_e32 v165, v2
	v_mul_f32_e32 v2, 0xbfb8aa3b, v154
	v_lshlrev_b32_e32 v137, 8, v134
	v_lshlrev_b32_e32 v148, 4, v148
	v_exp_f32_e32 v2, v2
	v_mul_f32_e32 v6, 0xbfb8aa3b, v155
	v_or_b32_e32 v135, 1, v136
	v_add3_u32 v148, v0, v148, v137
	v_exp_f32_e32 v6, v6
	ds_write_b128 v148, v[138:141]
	v_bitop3_b32 v138, v146, v135, v147 bitop3:0x36
	v_and_b32_e32 v147, 0xffff0000, v54
	v_and_b32_e32 v146, 0xffff0000, v50
	v_pk_fma_f32 v[156:157], v[98:99], v[170:171], v[156:157] op_sel:[1,0,0]
	v_pk_fma_f32 v[152:153], v[110:111], v[150:151], v[114:115] op_sel:[1,0,1]
	v_pk_mul_f32 v[158:159], v[158:159], v[164:165]
	v_pk_mov_b32 v[164:165], v[150:151], v[146:147] op_sel:[1,0]
	v_pk_fma_f32 v[150:151], v[102:103], v[150:151], v[156:157] op_sel:[1,0,0]
	v_add_f32_e32 v2, 1.0, v2
	v_pk_fma_f32 v[150:151], v[106:107], v[164:165], v[150:151] op_sel:[1,0,0]
	v_rcp_f32_e32 v160, v2
	v_add_f32_e32 v2, 1.0, v6
	v_mul_f32_e32 v6, 0xbfb8aa3b, v150
	v_exp_f32_e32 v6, v6
	v_mul_f32_e32 v10, 0xbfb8aa3b, v151
	v_exp_f32_e32 v10, v10
	v_rcp_f32_e32 v161, v2
	v_add_f32_e32 v2, 1.0, v6
	v_rcp_f32_e32 v156, v2
	v_add_f32_e32 v2, 1.0, v10
	v_rcp_f32_e32 v157, v2
	v_lshlrev_b32_e32 v138, 4, v138
	v_add3_u32 v137, v0, v138, v137
	v_and_b32_e32 v139, 0xffff0000, v66
	v_and_b32_e32 v138, 0xffff0000, v58
	v_pk_fma_f32 v[152:153], v[98:99], v[164:165], v[152:153] op_sel:[1,0,0]
	v_pk_fma_f32 v[148:149], v[110:111], v[146:147], v[114:115] op_sel:[1,0,1]
	v_pk_mul_f32 v[150:151], v[150:151], v[156:157]
	v_pk_mov_b32 v[156:157], v[146:147], v[138:139] op_sel:[1,0]
	v_pk_fma_f32 v[146:147], v[102:103], v[146:147], v[152:153] op_sel:[1,0,0]
	v_pk_fma_f32 v[148:149], v[98:99], v[156:157], v[148:149] op_sel:[1,0,0]
	v_pk_fma_f32 v[146:147], v[106:107], v[156:157], v[146:147] op_sel:[1,0,0]
	v_and_b32_e32 v141, 0xffff0000, v62
	v_mul_f32_e32 v2, 0xbfb8aa3b, v146
	v_exp_f32_e32 v2, v2
	v_mul_f32_e32 v6, 0xbfb8aa3b, v147
	v_exp_f32_e32 v6, v6
	v_mov_b32_e32 v140, v139
	v_add_f32_e32 v2, 1.0, v2
	v_pk_fma_f32 v[148:149], v[102:103], v[138:139], v[148:149] op_sel:[1,0,0]
	v_rcp_f32_e32 v152, v2
	v_add_f32_e32 v2, 1.0, v6
	v_pk_fma_f32 v[148:149], v[106:107], v[140:141], v[148:149] op_sel:[1,0,0]
	v_rcp_f32_e32 v153, v2
	v_mul_f32_e32 v2, 0xbfb8aa3b, v148
	v_exp_f32_e32 v2, v2
	v_mul_f32_e32 v6, 0xbfb8aa3b, v149
	v_exp_f32_e32 v6, v6
	v_pk_fma_f32 v[110:111], v[110:111], v[138:139], v[114:115] op_sel:[1,0,1]
	ds_write_b128 v137, v[142:145]
	v_and_b32_e32 v143, 0xffff0000, v70
	v_mov_b32_e32 v142, v141
	v_pk_fma_f32 v[98:99], v[98:99], v[140:141], v[110:111] op_sel:[1,0,0]
	v_and_b32_e32 v145, 0xffff0000, v74
	v_mov_b32_e32 v144, v143
	v_pk_fma_f32 v[98:99], v[102:103], v[142:143], v[98:99] op_sel:[1,0,0]
	v_add_f32_e32 v2, 1.0, v2
	v_pk_fma_f32 v[98:99], v[106:107], v[144:145], v[98:99] op_sel:[1,0,0]
	v_pk_mul_f32 v[146:147], v[146:147], v[152:153]
	v_rcp_f32_e32 v152, v2
	v_add_f32_e32 v2, 1.0, v6
	v_mul_f32_e32 v6, 0xbfb8aa3b, v98
	v_exp_f32_e32 v6, v6
	v_mul_f32_e32 v10, 0xbfb8aa3b, v99
	v_exp_f32_e32 v10, v10
	v_rcp_f32_e32 v153, v2
	v_add_f32_e32 v2, 1.0, v6
	v_rcp_f32_e32 v102, v2
	v_add_f32_e32 v2, 1.0, v10
	v_pk_mul_f32 v[154:155], v[154:155], v[160:161]
	v_rcp_f32_e32 v103, v2
	v_pk_mul_f32 v[154:155], v[154:155], v[126:127]
	v_add_u32_e32 v2, 1, v134
	v_pk_mul_f32 v[158:159], v[158:159], v[118:119]
	v_cvt_pk_bf16_f32 v141, v154, v155
	v_lshlrev_b32_e32 v10, 2, v2
	v_lshlrev_b32_e32 v154, 16, v3
	v_lshlrev_b32_e32 v155, 16, v15
	v_lshlrev_b32_e32 v156, 16, v7
	v_lshlrev_b32_e32 v157, 16, v11
	v_cvt_pk_bf16_f32 v140, v158, v159
	v_lshlrev_b32_e32 v6, 8, v2
	v_and_b32_e32 v10, 12, v10
	v_bfe_u32 v2, v2, 2, 2
	v_pk_fma_f32 v[158:159], v[112:113], v[156:157], v[116:117] op_sel_hi:[0,1,0]
	v_pk_mov_b32 v[156:157], v[156:157], v[154:155] op_sel:[1,0]
	v_pk_mul_f32 v[110:111], v[148:149], v[152:153]
	v_pk_mul_f32 v[98:99], v[98:99], v[102:103]
	v_bitop3_b32 v14, v10, v136, v2 bitop3:0x36
	v_bitop3_b32 v2, v10, v135, v2 bitop3:0x36
	v_lshlrev_b32_e32 v153, 16, v23
	v_lshlrev_b32_e32 v152, 16, v19
	v_pk_fma_f32 v[156:157], v[100:101], v[156:157], v[158:159] op_sel_hi:[0,1,1]
	v_pk_mul_f32 v[150:151], v[150:151], v[128:129]
	v_pk_mul_f32 v[106:107], v[146:147], v[122:123]
	v_pk_mul_f32 v[110:111], v[110:111], v[130:131]
	v_pk_mul_f32 v[98:99], v[98:99], v[132:133]
	v_lshlrev_b32_e32 v2, 4, v2
	v_pk_mov_b32 v[160:161], v[154:155], v[152:153] op_sel:[1,0]
	v_pk_fma_f32 v[156:157], v[104:105], v[154:155], v[156:157] op_sel_hi:[0,1,1]
	v_cvt_pk_bf16_f32 v142, v150, v151
	v_cvt_pk_bf16_f32 v143, v106, v107
	v_cvt_pk_bf16_f32 v144, v110, v111
	v_cvt_pk_bf16_f32 v145, v98, v99
	v_add3_u32 v2, v0, v2, v6
	v_pk_fma_f32 v[156:157], v[108:109], v[160:161], v[156:157] op_sel_hi:[0,1,1]
	v_lshlrev_b32_e32 v14, 4, v14
	ds_write_b128 v2, v[142:145]
	v_mul_f32_e32 v2, 0xbfb8aa3b, v156
	v_add3_u32 v14, v0, v14, v6
	v_exp_f32_e32 v2, v2
	v_mul_f32_e32 v6, 0xbfb8aa3b, v157
	v_exp_f32_e32 v6, v6
	v_pk_fma_f32 v[154:155], v[112:113], v[154:155], v[116:117] op_sel_hi:[0,1,0]
	v_lshlrev_b32_e32 v149, 16, v31
	v_lshlrev_b32_e32 v148, 16, v27
	v_pk_fma_f32 v[154:155], v[100:101], v[160:161], v[154:155] op_sel_hi:[0,1,1]
	v_cvt_pk_bf16_f32 v139, v162, v163
	v_pk_mov_b32 v[162:163], v[152:153], v[148:149] op_sel:[1,0]
	v_pk_fma_f32 v[154:155], v[104:105], v[152:153], v[154:155] op_sel_hi:[0,1,1]
	v_add_f32_e32 v2, 1.0, v2
	v_pk_fma_f32 v[154:155], v[108:109], v[162:163], v[154:155] op_sel_hi:[0,1,1]
	v_rcp_f32_e32 v158, v2
	v_add_f32_e32 v2, 1.0, v6
	v_mul_f32_e32 v6, 0xbfb8aa3b, v154
	v_exp_f32_e32 v6, v6
	v_mul_f32_e32 v10, 0xbfb8aa3b, v155
	v_rcp_f32_e32 v159, v2
	v_exp_f32_e32 v10, v10
	v_pk_fma_f32 v[152:153], v[112:113], v[152:153], v[116:117] op_sel_hi:[0,1,0]
	v_lshlrev_b32_e32 v145, 16, v39
	v_lshlrev_b32_e32 v144, 16, v35
	v_pk_fma_f32 v[152:153], v[100:101], v[162:163], v[152:153] op_sel_hi:[0,1,1]
	v_pk_fma_f32 v[150:151], v[112:113], v[148:149], v[116:117] op_sel_hi:[0,1,0]
	v_add_f32_e32 v2, 1.0, v6
	v_pk_mul_f32 v[156:157], v[156:157], v[158:159]
	v_pk_mov_b32 v[158:159], v[148:149], v[144:145] op_sel:[1,0]
	v_pk_fma_f32 v[148:149], v[104:105], v[148:149], v[152:153] op_sel_hi:[0,1,1]
	v_rcp_f32_e32 v160, v2
	v_add_f32_e32 v2, 1.0, v10
	v_pk_fma_f32 v[148:149], v[108:109], v[158:159], v[148:149] op_sel_hi:[0,1,1]
	v_rcp_f32_e32 v161, v2
	v_mul_f32_e32 v2, 0xbfb8aa3b, v148
	v_exp_f32_e32 v2, v2
	v_mul_f32_e32 v6, 0xbfb8aa3b, v149
	v_pk_mul_f32 v[166:167], v[166:167], v[120:121]
	v_exp_f32_e32 v6, v6
	v_cvt_pk_bf16_f32 v138, v166, v167
	ds_write_b128 v14, v[138:141]
	v_lshlrev_b32_e32 v141, 16, v47
	v_lshlrev_b32_e32 v140, 16, v43
	v_pk_fma_f32 v[150:151], v[100:101], v[158:159], v[150:151] op_sel_hi:[0,1,1]
	v_pk_fma_f32 v[146:147], v[112:113], v[144:145], v[116:117] op_sel_hi:[0,1,0]
	v_pk_mul_f32 v[154:155], v[154:155], v[160:161]
	v_add_f32_e32 v2, 1.0, v2
	v_pk_mov_b32 v[160:161], v[144:145], v[140:141] op_sel:[1,0]
	v_pk_fma_f32 v[144:145], v[104:105], v[144:145], v[150:151] op_sel_hi:[0,1,1]
	v_pk_mul_f32 v[152:153], v[154:155], v[124:125]
	v_rcp_f32_e32 v154, v2
	v_add_f32_e32 v2, 1.0, v6
	v_pk_fma_f32 v[144:145], v[108:109], v[160:161], v[144:145] op_sel_hi:[0,1,1]
	v_rcp_f32_e32 v155, v2
	v_mul_f32_e32 v2, 0xbfb8aa3b, v144
	v_exp_f32_e32 v2, v2
	v_mul_f32_e32 v6, 0xbfb8aa3b, v145
	v_exp_f32_e32 v6, v6
	v_lshlrev_b32_e32 v115, 16, v55
	v_lshlrev_b32_e32 v114, 16, v51
	v_pk_fma_f32 v[146:147], v[100:101], v[160:161], v[146:147] op_sel_hi:[0,1,1]
	v_pk_fma_f32 v[142:143], v[112:113], v[140:141], v[116:117] op_sel_hi:[0,1,0]
	v_pk_mul_f32 v[148:149], v[148:149], v[154:155]
	v_pk_mov_b32 v[154:155], v[140:141], v[114:115] op_sel:[1,0]
	v_pk_fma_f32 v[140:141], v[104:105], v[140:141], v[146:147] op_sel_hi:[0,1,1]
	v_add_f32_e32 v2, 1.0, v2
	v_pk_fma_f32 v[140:141], v[108:109], v[154:155], v[140:141] op_sel_hi:[0,1,1]
	v_rcp_f32_e32 v150, v2
	v_add_f32_e32 v2, 1.0, v6
	v_mul_f32_e32 v6, 0xbfb8aa3b, v140
	v_exp_f32_e32 v6, v6
	v_mul_f32_e32 v10, 0xbfb8aa3b, v141
	v_exp_f32_e32 v10, v10
	v_rcp_f32_e32 v151, v2
	v_add_f32_e32 v2, 1.0, v6
	v_rcp_f32_e32 v146, v2
	v_add_f32_e32 v2, 1.0, v10
	v_rcp_f32_e32 v147, v2
	v_lshlrev_b32_e32 v98, 16, v59
	v_lshlrev_b32_e32 v99, 16, v67
	v_pk_fma_f32 v[142:143], v[100:101], v[154:155], v[142:143] op_sel_hi:[0,1,1]
	v_pk_fma_f32 v[138:139], v[112:113], v[114:115], v[116:117] op_sel_hi:[0,1,0]
	v_pk_mul_f32 v[140:141], v[140:141], v[146:147]
	v_pk_mov_b32 v[146:147], v[114:115], v[98:99] op_sel:[1,0]
	v_pk_fma_f32 v[114:115], v[104:105], v[114:115], v[142:143] op_sel_hi:[0,1,1]
	v_pk_fma_f32 v[114:115], v[108:109], v[146:147], v[114:115] op_sel_hi:[0,1,1]
	v_mul_f32_e32 v2, 0xbfb8aa3b, v114
	v_exp_f32_e32 v2, v2
	v_mul_f32_e32 v6, 0xbfb8aa3b, v115
	v_exp_f32_e32 v6, v6
	v_pk_fma_f32 v[138:139], v[100:101], v[146:147], v[138:139] op_sel_hi:[0,1,1]
	v_lshlrev_b32_e32 v103, 16, v63
	v_mov_b32_e32 v102, v99
	v_add_f32_e32 v2, 1.0, v2
	v_pk_fma_f32 v[138:139], v[104:105], v[98:99], v[138:139] op_sel_hi:[0,1,1]
	v_pk_mul_f32 v[142:143], v[140:141], v[128:129]
	v_rcp_f32_e32 v140, v2
	v_add_f32_e32 v2, 1.0, v6
	v_pk_fma_f32 v[138:139], v[108:109], v[102:103], v[138:139] op_sel_hi:[0,1,1]
	v_rcp_f32_e32 v141, v2
	v_mul_f32_e32 v2, 0xbfb8aa3b, v138
	v_exp_f32_e32 v2, v2
	v_mul_f32_e32 v6, 0xbfb8aa3b, v139
	v_exp_f32_e32 v6, v6
	v_pk_fma_f32 v[98:99], v[112:113], v[98:99], v[116:117] op_sel_hi:[0,1,0]
	v_lshlrev_b32_e32 v111, 16, v71
	v_mov_b32_e32 v110, v103
	v_pk_fma_f32 v[98:99], v[100:101], v[102:103], v[98:99] op_sel_hi:[0,1,1]
	v_lshlrev_b32_e32 v107, 16, v75
	v_mov_b32_e32 v106, v111
	v_pk_fma_f32 v[98:99], v[104:105], v[110:111], v[98:99] op_sel_hi:[0,1,1]
	v_add_f32_e32 v2, 1.0, v2
	v_pk_fma_f32 v[98:99], v[108:109], v[106:107], v[98:99] op_sel_hi:[0,1,1]
	v_pk_mul_f32 v[114:115], v[114:115], v[140:141]
	v_rcp_f32_e32 v140, v2
	v_add_f32_e32 v2, 1.0, v6
	v_mul_f32_e32 v6, 0xbfb8aa3b, v98
	v_exp_f32_e32 v6, v6
	v_mul_f32_e32 v10, 0xbfb8aa3b, v99
	v_exp_f32_e32 v10, v10
	v_rcp_f32_e32 v141, v2
	v_add_f32_e32 v2, 1.0, v6
	v_rcp_f32_e32 v102, v2
	v_add_f32_e32 v2, 1.0, v10
	v_rcp_f32_e32 v103, v2
	v_add_u32_e32 v2, 2, v134
	v_lshlrev_b32_e32 v10, 2, v2
	v_lshlrev_b32_e32 v6, 8, v2
	v_and_b32_e32 v10, 12, v10
	v_bfe_u32 v2, v2, 2, 2
	v_pk_mul_f32 v[144:145], v[144:145], v[150:151]
	v_pk_mul_f32 v[110:111], v[138:139], v[140:141]
	v_pk_mul_f32 v[98:99], v[98:99], v[102:103]
	v_bitop3_b32 v14, v10, v136, v2 bitop3:0x36
	v_bitop3_b32 v2, v10, v135, v2 bitop3:0x36
	v_pk_mul_f32 v[156:157], v[156:157], v[120:121]
	v_pk_mul_f32 v[148:149], v[148:149], v[118:119]
	v_pk_mul_f32 v[144:145], v[144:145], v[126:127]
	v_pk_mul_f32 v[106:107], v[114:115], v[122:123]
	v_pk_mul_f32 v[110:111], v[110:111], v[130:131]
	v_pk_mul_f32 v[98:99], v[98:99], v[132:133]
	v_lshlrev_b32_e32 v14, 4, v14
	v_lshlrev_b32_e32 v2, 4, v2
	v_cvt_pk_bf16_f32 v138, v156, v157
	v_cvt_pk_bf16_f32 v139, v152, v153
	v_cvt_pk_bf16_f32 v140, v148, v149
	v_cvt_pk_bf16_f32 v141, v144, v145
	v_cvt_pk_bf16_f32 v142, v142, v143
	v_cvt_pk_bf16_f32 v143, v106, v107
	v_cvt_pk_bf16_f32 v144, v110, v111
	v_cvt_pk_bf16_f32 v145, v98, v99
	v_add3_u32 v14, v0, v14, v6
	v_add3_u32 v2, v0, v2, v6
	ds_write_b128 v14, v[138:141]
	ds_write_b128 v2, v[142:145]
	v_mov_b32_e32 v2, v113
	v_mov_b32_e32 v6, v117
	v_and_b32_e32 v15, 0xffff0000, v15
	v_and_b32_e32 v14, 0xffff0000, v3
	v_and_b32_e32 v11, 0xffff0000, v11
	v_and_b32_e32 v10, 0xffff0000, v7
	v_and_b32_e32 v22, 0xffff0000, v19
	v_pk_fma_f32 v[18:19], v[2:3], v[10:11], v[6:7] op_sel_hi:[0,1,0]
	v_mov_b32_e32 v100, v101
	v_pk_mov_b32 v[10:11], v[10:11], v[14:15] op_sel:[1,0]
	v_and_b32_e32 v23, 0xffff0000, v23
	v_pk_fma_f32 v[10:11], v[100:101], v[10:11], v[18:19] op_sel_hi:[0,1,1]
	v_mov_b32_e32 v18, v105
	v_mov_b32_e32 v74, v109
	v_pk_mov_b32 v[98:99], v[14:15], v[22:23] op_sel:[1,0]
	v_pk_fma_f32 v[10:11], v[18:19], v[14:15], v[10:11] op_sel_hi:[0,1,1]
	v_and_b32_e32 v55, 0xffff0000, v55
	v_and_b32_e32 v54, 0xffff0000, v51
	v_and_b32_e32 v47, 0xffff0000, v47
	v_and_b32_e32 v46, 0xffff0000, v43
	v_and_b32_e32 v39, 0xffff0000, v39
	v_and_b32_e32 v38, 0xffff0000, v35
	v_and_b32_e32 v31, 0xffff0000, v31
	v_and_b32_e32 v30, 0xffff0000, v27
	v_pk_fma_f32 v[10:11], v[74:75], v[98:99], v[10:11] op_sel_hi:[0,1,1]
	v_pk_fma_f32 v[50:51], v[2:3], v[54:55], v[6:7] op_sel_hi:[0,1,0]
	v_pk_fma_f32 v[42:43], v[2:3], v[46:47], v[6:7] op_sel_hi:[0,1,0]
	v_pk_fma_f32 v[34:35], v[2:3], v[38:39], v[6:7] op_sel_hi:[0,1,0]
	v_pk_fma_f32 v[26:27], v[2:3], v[30:31], v[6:7] op_sel_hi:[0,1,0]
	v_mul_f32_e32 v3, 0xbfb8aa3b, v10
	v_mul_f32_e32 v7, 0xbfb8aa3b, v11
	v_exp_f32_e32 v3, v3
	v_exp_f32_e32 v7, v7
	v_pk_mov_b32 v[104:105], v[22:23], v[30:31] op_sel:[1,0]
	v_and_b32_e32 v67, 0xffff0000, v67
	v_and_b32_e32 v66, 0xffff0000, v59
	v_pk_fma_f32 v[14:15], v[2:3], v[14:15], v[6:7] op_sel_hi:[0,1,0]
	v_pk_fma_f32 v[14:15], v[100:101], v[98:99], v[14:15] op_sel_hi:[0,1,1]
	v_pk_fma_f32 v[14:15], v[18:19], v[22:23], v[14:15] op_sel_hi:[0,1,1]
	v_add_f32_e32 v3, 1.0, v3
	v_pk_fma_f32 v[14:15], v[74:75], v[104:105], v[14:15] op_sel_hi:[0,1,1]
	v_rcp_f32_e32 v102, v3
	v_add_f32_e32 v3, 1.0, v7
	v_mul_f32_e32 v7, 0xbfb8aa3b, v14
	v_exp_f32_e32 v7, v7
	v_mul_f32_e32 v19, 0xbfb8aa3b, v15
	v_exp_f32_e32 v19, v19
	v_rcp_f32_e32 v103, v3
	v_add_f32_e32 v3, 1.0, v7
	v_rcp_f32_e32 v98, v3
	v_add_f32_e32 v3, 1.0, v19
	v_rcp_f32_e32 v99, v3
	v_pk_fma_f32 v[22:23], v[2:3], v[22:23], v[6:7] op_sel_hi:[0,1,0]
	v_pk_fma_f32 v[22:23], v[100:101], v[104:105], v[22:23] op_sel_hi:[0,1,1]
	v_pk_fma_f32 v[22:23], v[18:19], v[30:31], v[22:23] op_sel_hi:[0,1,1]
	v_pk_mul_f32 v[14:15], v[14:15], v[98:99]
	v_pk_mov_b32 v[98:99], v[30:31], v[38:39] op_sel:[1,0]
	v_pk_mul_f32 v[10:11], v[10:11], v[102:103]
	v_pk_fma_f32 v[22:23], v[74:75], v[98:99], v[22:23] op_sel_hi:[0,1,1]
	v_mul_f32_e32 v3, 0xbfb8aa3b, v22
	v_exp_f32_e32 v3, v3
	v_mul_f32_e32 v7, 0xbfb8aa3b, v23
	v_exp_f32_e32 v7, v7
	v_pk_fma_f32 v[26:27], v[100:101], v[98:99], v[26:27] op_sel_hi:[0,1,1]
	v_add_f32_e32 v3, 1.0, v3
	v_pk_mov_b32 v[102:103], v[38:39], v[46:47] op_sel:[1,0]
	v_pk_fma_f32 v[26:27], v[18:19], v[38:39], v[26:27] op_sel_hi:[0,1,1]
	v_rcp_f32_e32 v30, v3
	v_add_f32_e32 v3, 1.0, v7
	v_pk_fma_f32 v[26:27], v[74:75], v[102:103], v[26:27] op_sel_hi:[0,1,1]
	v_rcp_f32_e32 v31, v3
	v_mul_f32_e32 v3, 0xbfb8aa3b, v26
	v_exp_f32_e32 v3, v3
	v_mul_f32_e32 v7, 0xbfb8aa3b, v27
	v_exp_f32_e32 v7, v7
	v_pk_fma_f32 v[34:35], v[100:101], v[102:103], v[34:35] op_sel_hi:[0,1,1]
	v_pk_mov_b32 v[38:39], v[46:47], v[54:55] op_sel:[1,0]
	v_pk_fma_f32 v[34:35], v[18:19], v[46:47], v[34:35] op_sel_hi:[0,1,1]
	v_add_f32_e32 v3, 1.0, v3
	v_pk_fma_f32 v[34:35], v[74:75], v[38:39], v[34:35] op_sel_hi:[0,1,1]
	v_pk_mul_f32 v[22:23], v[22:23], v[30:31]
	v_rcp_f32_e32 v30, v3
	v_add_f32_e32 v3, 1.0, v7
	v_mul_f32_e32 v7, 0xbfb8aa3b, v34
	v_exp_f32_e32 v7, v7
	v_mul_f32_e32 v19, 0xbfb8aa3b, v35
	v_exp_f32_e32 v19, v19
	v_rcp_f32_e32 v31, v3
	v_add_f32_e32 v3, 1.0, v7
	v_rcp_f32_e32 v46, v3
	v_add_f32_e32 v3, 1.0, v19
	v_rcp_f32_e32 v47, v3
	v_pk_fma_f32 v[38:39], v[100:101], v[38:39], v[42:43] op_sel_hi:[0,1,1]
	v_pk_mul_f32 v[26:27], v[26:27], v[30:31]
	v_pk_fma_f32 v[38:39], v[18:19], v[54:55], v[38:39] op_sel_hi:[0,1,1]
	v_pk_mul_f32 v[30:31], v[34:35], v[46:47]
	v_pk_mov_b32 v[34:35], v[54:55], v[66:67] op_sel:[1,0]
	v_and_b32_e32 v59, 0xffff0000, v63
	v_pk_fma_f32 v[38:39], v[74:75], v[34:35], v[38:39] op_sel_hi:[0,1,1]
	v_mul_f32_e32 v3, 0xbfb8aa3b, v38
	v_exp_f32_e32 v3, v3
	v_mul_f32_e32 v7, 0xbfb8aa3b, v39
	v_exp_f32_e32 v7, v7
	v_pk_fma_f32 v[34:35], v[100:101], v[34:35], v[50:51] op_sel_hi:[0,1,1]
	v_mov_b32_e32 v58, v67
	v_add_f32_e32 v3, 1.0, v3
	v_pk_fma_f32 v[34:35], v[18:19], v[66:67], v[34:35] op_sel_hi:[0,1,1]
	v_rcp_f32_e32 v42, v3
	v_add_f32_e32 v3, 1.0, v7
	v_pk_fma_f32 v[34:35], v[74:75], v[58:59], v[34:35] op_sel_hi:[0,1,1]
	v_rcp_f32_e32 v43, v3
	v_mul_f32_e32 v3, 0xbfb8aa3b, v34
	v_mul_f32_e32 v7, 0xbfb8aa3b, v35
	v_exp_f32_e32 v3, v3
	v_exp_f32_e32 v7, v7
	v_pk_mul_f32 v[38:39], v[38:39], v[42:43]
	v_and_b32_e32 v63, 0xffff0000, v71
	v_add_f32_e32 v3, 1.0, v3
	v_add_f32_e32 v7, 1.0, v7
	v_rcp_f32_e32 v42, v3
	v_pk_fma_f32 v[2:3], v[2:3], v[66:67], v[6:7] op_sel_hi:[0,1,0]
	v_mov_b32_e32 v62, v59
	v_pk_fma_f32 v[2:3], v[100:101], v[58:59], v[2:3] op_sel_hi:[0,1,1]
	v_lshlrev_b32_e32 v54, 16, v4
	v_lshlrev_b32_e32 v55, 16, v16
	v_lshlrev_b32_e32 v59, 16, v12
	v_lshlrev_b32_e32 v58, 16, v8
	v_mov_b32_e32 v70, v63
	v_pk_fma_f32 v[2:3], v[18:19], v[62:63], v[2:3] op_sel_hi:[0,1,1]
	v_pk_fma_f32 v[62:63], v[90:91], v[58:59], v[94:95] op_sel_hi:[0,1,0]
	v_pk_mov_b32 v[58:59], v[58:59], v[54:55] op_sel:[1,0]
	v_lshlrev_b32_e32 v51, 16, v24
	v_lshlrev_b32_e32 v50, 16, v20
	v_pk_fma_f32 v[58:59], v[78:79], v[58:59], v[62:63] op_sel_hi:[0,1,1]
	v_pk_mov_b32 v[66:67], v[54:55], v[50:51] op_sel:[1,0]
	v_pk_fma_f32 v[58:59], v[82:83], v[54:55], v[58:59] op_sel_hi:[0,1,1]
	v_pk_mul_f32 v[10:11], v[10:11], v[120:121]
	v_rcp_f32_e32 v43, v7
	v_pk_fma_f32 v[58:59], v[86:87], v[66:67], v[58:59] op_sel_hi:[0,1,1]
	v_cvt_pk_bf16_f32 v98, v10, v11
	v_mul_f32_e32 v10, 0xbfb8aa3b, v58
	v_exp_f32_e32 v10, v10
	v_mul_f32_e32 v62, 0xbfb8aa3b, v59
	v_exp_f32_e32 v63, v62
	v_pk_fma_f32 v[54:55], v[90:91], v[54:55], v[94:95] op_sel_hi:[0,1,0]
	v_and_b32_e32 v71, 0xffff0000, v75
	v_pk_mul_f32 v[34:35], v[34:35], v[42:43]
	v_lshlrev_b32_e32 v43, 16, v32
	v_lshlrev_b32_e32 v42, 16, v28
	v_pk_fma_f32 v[54:55], v[78:79], v[66:67], v[54:55] op_sel_hi:[0,1,1]
	v_pk_fma_f32 v[2:3], v[74:75], v[70:71], v[2:3] op_sel_hi:[0,1,1]
	v_pk_mov_b32 v[70:71], v[50:51], v[42:43] op_sel:[1,0]
	v_pk_fma_f32 v[54:55], v[82:83], v[50:51], v[54:55] op_sel_hi:[0,1,1]
	v_add_f32_e32 v10, 1.0, v10
	v_pk_fma_f32 v[54:55], v[86:87], v[70:71], v[54:55] op_sel_hi:[0,1,1]
	v_rcp_f32_e32 v62, v10
	v_add_f32_e32 v10, 1.0, v63
	v_mul_f32_e32 v63, 0xbfb8aa3b, v54
	v_exp_f32_e32 v66, v63
	v_mul_f32_e32 v63, 0xbfb8aa3b, v55
	v_exp_f32_e32 v67, v63
	v_rcp_f32_e32 v63, v10
	v_pk_mul_f32 v[34:35], v[34:35], v[130:131]
	v_add_f32_e32 v10, 1.0, v66
	v_pk_fma_f32 v[50:51], v[90:91], v[50:51], v[94:95] op_sel_hi:[0,1,0]
	v_cvt_pk_bf16_f32 v104, v34, v35
	v_lshlrev_b32_e32 v35, 16, v40
	v_lshlrev_b32_e32 v34, 16, v36
	v_rcp_f32_e32 v66, v10
	v_add_f32_e32 v10, 1.0, v67
	v_pk_fma_f32 v[50:51], v[78:79], v[70:71], v[50:51] op_sel_hi:[0,1,1]
	v_pk_fma_f32 v[46:47], v[90:91], v[42:43], v[94:95] op_sel_hi:[0,1,0]
	v_rcp_f32_e32 v67, v10
	v_pk_mul_f32 v[58:59], v[58:59], v[62:63]
	v_pk_mov_b32 v[62:63], v[42:43], v[34:35] op_sel:[1,0]
	v_pk_fma_f32 v[42:43], v[82:83], v[42:43], v[50:51] op_sel_hi:[0,1,1]
	v_pk_fma_f32 v[42:43], v[86:87], v[62:63], v[42:43] op_sel_hi:[0,1,1]
	v_mul_f32_e32 v10, 0xbfb8aa3b, v42
	v_exp_f32_e32 v10, v10
	v_mul_f32_e32 v50, 0xbfb8aa3b, v43
	v_pk_mul_f32 v[54:55], v[54:55], v[66:67]
	v_exp_f32_e32 v66, v50
	v_mul_f32_e32 v18, 0xbfb8aa3b, v3
	v_mul_f32_e32 v6, 0xbfb8aa3b, v2
	v_exp_f32_e32 v18, v18
	v_add_f32_e32 v10, 1.0, v10
	v_exp_f32_e32 v6, v6
	v_pk_mul_f32 v[50:51], v[54:55], v[124:125]
	v_rcp_f32_e32 v54, v10
	v_add_f32_e32 v10, 1.0, v66
	v_pk_mul_f32 v[26:27], v[26:27], v[126:127]
	v_rcp_f32_e32 v55, v10
	v_cvt_pk_bf16_f32 v101, v26, v27
	v_lshlrev_b32_e32 v27, 16, v48
	v_lshlrev_b32_e32 v26, 16, v44
	v_pk_fma_f32 v[46:47], v[78:79], v[62:63], v[46:47] op_sel_hi:[0,1,1]
	v_add_f32_e32 v7, 1.0, v18
	v_pk_mul_f32 v[18:19], v[38:39], v[122:123]
	v_pk_fma_f32 v[38:39], v[90:91], v[34:35], v[94:95] op_sel_hi:[0,1,0]
	v_pk_mov_b32 v[66:67], v[34:35], v[26:27] op_sel:[1,0]
	v_pk_fma_f32 v[34:35], v[82:83], v[34:35], v[46:47] op_sel_hi:[0,1,1]
	v_pk_mul_f32 v[30:31], v[30:31], v[128:129]
	v_add_f32_e32 v6, 1.0, v6
	v_cvt_pk_bf16_f32 v103, v18, v19
	v_lshlrev_b32_e32 v19, 16, v56
	v_lshlrev_b32_e32 v18, 16, v52
	v_pk_fma_f32 v[34:35], v[86:87], v[66:67], v[34:35] op_sel_hi:[0,1,1]
	v_pk_fma_f32 v[38:39], v[78:79], v[66:67], v[38:39] op_sel_hi:[0,1,1]
	v_rcp_f32_e32 v6, v6
	v_rcp_f32_e32 v7, v7
	v_cvt_pk_bf16_f32 v102, v30, v31
	v_pk_fma_f32 v[30:31], v[90:91], v[26:27], v[94:95] op_sel_hi:[0,1,0]
	v_mul_f32_e32 v10, 0xbfb8aa3b, v34
	v_pk_mul_f32 v[42:43], v[42:43], v[54:55]
	v_pk_mov_b32 v[54:55], v[26:27], v[18:19] op_sel:[1,0]
	v_pk_fma_f32 v[26:27], v[82:83], v[26:27], v[38:39] op_sel_hi:[0,1,1]
	v_exp_f32_e32 v10, v10
	v_mul_f32_e32 v46, 0xbfb8aa3b, v35
	v_pk_fma_f32 v[26:27], v[86:87], v[54:55], v[26:27] op_sel_hi:[0,1,1]
	v_exp_f32_e32 v47, v46
	v_mul_f32_e32 v38, 0xbfb8aa3b, v26
	v_exp_f32_e32 v38, v38
	v_mul_f32_e32 v39, 0xbfb8aa3b, v27
	v_pk_mul_f32 v[2:3], v[2:3], v[6:7]
	v_exp_f32_e32 v39, v39
	v_pk_mul_f32 v[2:3], v[2:3], v[132:133]
	v_add_f32_e32 v10, 1.0, v10
	v_cvt_pk_bf16_f32 v105, v2, v3
	v_add_u32_e32 v2, 3, v134
	v_rcp_f32_e32 v46, v10
	v_add_f32_e32 v10, 1.0, v47
	v_lshlrev_b32_e32 v6, 2, v2
	v_rcp_f32_e32 v47, v10
	v_add_f32_e32 v10, 1.0, v38
	v_lshlrev_b32_e32 v3, 8, v2
	v_and_b32_e32 v6, 12, v6
	v_bfe_u32 v2, v2, 2, 2
	v_rcp_f32_e32 v38, v10
	v_add_f32_e32 v10, 1.0, v39
	v_bitop3_b32 v7, v6, v136, v2 bitop3:0x36
	v_bitop3_b32 v2, v6, v135, v2 bitop3:0x36
	v_rcp_f32_e32 v39, v10
	v_lshlrev_b32_e32 v2, 4, v2
	v_lshlrev_b32_e32 v7, 4, v7
	v_add3_u32 v2, v0, v2, v3
	v_pk_mul_f32 v[22:23], v[22:23], v[118:119]
	v_add3_u32 v7, v0, v7, v3
	ds_write_b128 v2, v[102:105]
	v_lshlrev_b32_e32 v2, 16, v60
	v_lshlrev_b32_e32 v3, 16, v68
	v_pk_fma_f32 v[30:31], v[78:79], v[54:55], v[30:31] op_sel_hi:[0,1,1]
	v_cvt_pk_bf16_f32 v100, v22, v23
	v_pk_fma_f32 v[22:23], v[90:91], v[18:19], v[94:95] op_sel_hi:[0,1,0]
	v_pk_mul_f32 v[26:27], v[26:27], v[38:39]
	v_pk_mov_b32 v[38:39], v[18:19], v[2:3] op_sel:[1,0]
	v_pk_fma_f32 v[18:19], v[82:83], v[18:19], v[30:31] op_sel_hi:[0,1,1]
	v_pk_fma_f32 v[18:19], v[86:87], v[38:39], v[18:19] op_sel_hi:[0,1,1]
	v_mul_f32_e32 v10, 0xbfb8aa3b, v18
	v_exp_f32_e32 v10, v10
	v_mul_f32_e32 v30, 0xbfb8aa3b, v19
	v_exp_f32_e32 v31, v30
	v_pk_mul_f32 v[14:15], v[14:15], v[124:125]
	v_pk_fma_f32 v[22:23], v[78:79], v[38:39], v[22:23] op_sel_hi:[0,1,1]
	v_cvt_pk_bf16_f32 v99, v14, v15
	ds_write_b128 v7, v[98:101]
	v_lshlrev_b32_e32 v7, 16, v64
	v_mov_b32_e32 v6, v3
	v_add_f32_e32 v10, 1.0, v10
	v_pk_fma_f32 v[22:23], v[82:83], v[2:3], v[22:23] op_sel_hi:[0,1,1]
	v_rcp_f32_e32 v30, v10
	v_add_f32_e32 v10, 1.0, v31
	v_pk_fma_f32 v[22:23], v[86:87], v[6:7], v[22:23] op_sel_hi:[0,1,1]
	v_rcp_f32_e32 v31, v10
	v_mul_f32_e32 v10, 0xbfb8aa3b, v22
	v_mul_f32_e32 v38, 0xbfb8aa3b, v23
	v_exp_f32_e32 v10, v10
	v_exp_f32_e32 v38, v38
	v_pk_mul_f32 v[18:19], v[18:19], v[30:31]
	v_pk_fma_f32 v[2:3], v[90:91], v[2:3], v[94:95] op_sel_hi:[0,1,0]
	v_add_f32_e32 v10, 1.0, v10
	v_add_f32_e32 v31, 1.0, v38
	v_rcp_f32_e32 v30, v10
	v_rcp_f32_e32 v31, v31
	v_lshlrev_b32_e32 v15, 16, v72
	v_mov_b32_e32 v14, v7
	v_pk_mul_f32 v[26:27], v[26:27], v[128:129]
	v_pk_fma_f32 v[2:3], v[78:79], v[6:7], v[2:3] op_sel_hi:[0,1,1]
	v_mov_b32_e32 v10, v15
	v_pk_fma_f32 v[2:3], v[82:83], v[14:15], v[2:3] op_sel_hi:[0,1,1]
	v_pk_mul_f32 v[14:15], v[22:23], v[30:31]
	v_cvt_pk_bf16_f32 v102, v26, v27
	v_mov_b32_e32 v22, v91
	v_mov_b32_e32 v26, v95
	v_and_b32_e32 v63, 0xffff0000, v16
	v_and_b32_e32 v62, 0xffff0000, v4
	v_and_b32_e32 v67, 0xffff0000, v12
	v_and_b32_e32 v66, 0xffff0000, v8
	v_pk_mul_f32 v[58:59], v[58:59], v[120:121]
	v_pk_fma_f32 v[70:71], v[22:23], v[66:67], v[26:27] op_sel_hi:[0,1,0]
	v_mov_b32_e32 v8, v79
	v_pk_mov_b32 v[66:67], v[66:67], v[62:63] op_sel:[1,0]
	v_cvt_pk_bf16_f32 v98, v58, v59
	v_and_b32_e32 v59, 0xffff0000, v24
	v_and_b32_e32 v58, 0xffff0000, v20
	v_pk_fma_f32 v[66:67], v[8:9], v[66:67], v[70:71] op_sel_hi:[0,1,1]
	v_mov_b32_e32 v12, v83
	v_mov_b32_e32 v4, v87
	v_pk_mov_b32 v[74:75], v[62:63], v[58:59] op_sel:[1,0]
	v_pk_fma_f32 v[66:67], v[12:13], v[62:63], v[66:67] op_sel_hi:[0,1,1]
	v_pk_fma_f32 v[66:67], v[4:5], v[74:75], v[66:67] op_sel_hi:[0,1,1]
	v_mul_f32_e32 v16, 0xbfb8aa3b, v66
	v_pk_fma_f32 v[62:63], v[22:23], v[62:63], v[26:27] op_sel_hi:[0,1,0]
	v_pk_mul_f32 v[34:35], v[34:35], v[46:47]
	v_cvt_pk_bf16_f32 v99, v50, v51
	v_and_b32_e32 v51, 0xffff0000, v32
	v_and_b32_e32 v50, 0xffff0000, v28
	v_exp_f32_e32 v16, v16
	v_mul_f32_e32 v20, 0xbfb8aa3b, v67
	v_pk_fma_f32 v[62:63], v[8:9], v[74:75], v[62:63] op_sel_hi:[0,1,1]
	v_lshlrev_b32_e32 v11, 16, v76
	v_pk_mul_f32 v[42:43], v[42:43], v[118:119]
	v_pk_mul_f32 v[34:35], v[34:35], v[126:127]
	v_exp_f32_e32 v20, v20
	v_pk_mov_b32 v[78:79], v[58:59], v[50:51] op_sel:[1,0]
	v_pk_fma_f32 v[62:63], v[12:13], v[58:59], v[62:63] op_sel_hi:[0,1,1]
	v_pk_fma_f32 v[2:3], v[86:87], v[10:11], v[2:3] op_sel_hi:[0,1,1]
	v_pk_mul_f32 v[10:11], v[18:19], v[122:123]
	v_cvt_pk_bf16_f32 v100, v42, v43
	v_cvt_pk_bf16_f32 v101, v34, v35
	v_and_b32_e32 v19, 0xffff0000, v56
	v_and_b32_e32 v18, 0xffff0000, v52
	v_and_b32_e32 v35, 0xffff0000, v48
	v_and_b32_e32 v34, 0xffff0000, v44
	v_and_b32_e32 v43, 0xffff0000, v40
	v_and_b32_e32 v42, 0xffff0000, v36
	v_pk_fma_f32 v[62:63], v[4:5], v[78:79], v[62:63] op_sel_hi:[0,1,1]
	v_pk_fma_f32 v[30:31], v[22:23], v[18:19], v[26:27] op_sel_hi:[0,1,0]
	v_pk_fma_f32 v[38:39], v[22:23], v[34:35], v[26:27] op_sel_hi:[0,1,0]
	v_pk_fma_f32 v[46:47], v[22:23], v[42:43], v[26:27] op_sel_hi:[0,1,0]
	v_pk_fma_f32 v[54:55], v[22:23], v[50:51], v[26:27] op_sel_hi:[0,1,0]
	v_mul_f32_e32 v23, 0xbfb8aa3b, v63
	v_add_f32_e32 v16, 1.0, v16
	v_exp_f32_e32 v23, v23
	v_rcp_f32_e32 v70, v16
	v_add_f32_e32 v16, 1.0, v20
	v_mul_f32_e32 v20, 0xbfb8aa3b, v62
	v_exp_f32_e32 v20, v20
	v_rcp_f32_e32 v71, v16
	v_pk_fma_f32 v[58:59], v[22:23], v[58:59], v[26:27] op_sel_hi:[0,1,0]
	v_pk_fma_f32 v[58:59], v[8:9], v[78:79], v[58:59] op_sel_hi:[0,1,1]
	v_add_f32_e32 v16, 1.0, v20
	v_pk_mul_f32 v[66:67], v[66:67], v[70:71]
	v_pk_mov_b32 v[70:71], v[50:51], v[42:43] op_sel:[1,0]
	v_pk_fma_f32 v[50:51], v[12:13], v[50:51], v[58:59] op_sel_hi:[0,1,1]
	v_rcp_f32_e32 v74, v16
	v_add_f32_e32 v16, 1.0, v23
	v_pk_fma_f32 v[50:51], v[4:5], v[70:71], v[50:51] op_sel_hi:[0,1,1]
	v_rcp_f32_e32 v75, v16
	v_mul_f32_e32 v16, 0xbfb8aa3b, v50
	v_exp_f32_e32 v16, v16
	v_mul_f32_e32 v20, 0xbfb8aa3b, v51
	v_exp_f32_e32 v20, v20
	v_pk_fma_f32 v[54:55], v[8:9], v[70:71], v[54:55] op_sel_hi:[0,1,1]
	v_mul_f32_e32 v6, 0xbfb8aa3b, v2
	v_mul_f32_e32 v7, 0xbfb8aa3b, v3
	v_pk_mul_f32 v[62:63], v[62:63], v[74:75]
	v_add_f32_e32 v16, 1.0, v16
	v_pk_mov_b32 v[74:75], v[42:43], v[34:35] op_sel:[1,0]
	v_pk_fma_f32 v[42:43], v[12:13], v[42:43], v[54:55] op_sel_hi:[0,1,1]
	v_exp_f32_e32 v6, v6
	v_exp_f32_e32 v7, v7
	v_pk_mul_f32 v[58:59], v[62:63], v[124:125]
	v_rcp_f32_e32 v62, v16
	v_add_f32_e32 v16, 1.0, v20
	v_pk_fma_f32 v[42:43], v[4:5], v[74:75], v[42:43] op_sel_hi:[0,1,1]
	v_rcp_f32_e32 v63, v16
	v_mul_f32_e32 v16, 0xbfb8aa3b, v42
	v_exp_f32_e32 v16, v16
	v_mul_f32_e32 v20, 0xbfb8aa3b, v43
	v_exp_f32_e32 v20, v20
	v_add_f32_e32 v6, 1.0, v6
	v_add_f32_e32 v7, 1.0, v7
	v_pk_fma_f32 v[46:47], v[8:9], v[74:75], v[46:47] op_sel_hi:[0,1,1]
	v_rcp_f32_e32 v6, v6
	v_rcp_f32_e32 v7, v7
	v_pk_mul_f32 v[50:51], v[50:51], v[62:63]
	v_pk_mov_b32 v[62:63], v[34:35], v[18:19] op_sel:[1,0]
	v_pk_fma_f32 v[34:35], v[12:13], v[34:35], v[46:47] op_sel_hi:[0,1,1]
	v_add_f32_e32 v16, 1.0, v16
	v_pk_fma_f32 v[34:35], v[4:5], v[62:63], v[34:35] op_sel_hi:[0,1,1]
	v_rcp_f32_e32 v54, v16
	v_add_f32_e32 v16, 1.0, v20
	v_mul_f32_e32 v20, 0xbfb8aa3b, v34
	v_exp_f32_e32 v20, v20
	v_mul_f32_e32 v23, 0xbfb8aa3b, v35
	v_pk_mul_f32 v[2:3], v[2:3], v[6:7]
	v_exp_f32_e32 v23, v23
	v_pk_mul_f32 v[2:3], v[2:3], v[132:133]
	v_rcp_f32_e32 v55, v16
	v_cvt_pk_bf16_f32 v105, v2, v3
	v_add_u32_e32 v2, 4, v134
	v_lshlrev_b32_e32 v6, 2, v2
	v_add_f32_e32 v16, 1.0, v20
	v_lshlrev_b32_e32 v3, 8, v2
	v_and_b32_e32 v6, 12, v6
	v_bfe_u32 v2, v2, 2, 2
	v_rcp_f32_e32 v46, v16
	v_add_f32_e32 v16, 1.0, v23
	v_bitop3_b32 v7, v6, v136, v2 bitop3:0x36
	v_bitop3_b32 v2, v6, v135, v2 bitop3:0x36
	v_rcp_f32_e32 v47, v16
	v_pk_mul_f32 v[14:15], v[14:15], v[130:131]
	v_lshlrev_b32_e32 v2, 4, v2
	v_cvt_pk_bf16_f32 v103, v10, v11
	v_cvt_pk_bf16_f32 v104, v14, v15
	v_lshlrev_b32_e32 v7, 4, v7
	v_add3_u32 v2, v0, v2, v3
	v_add3_u32 v7, v0, v7, v3
	ds_write_b128 v2, v[102:105]
	v_and_b32_e32 v3, 0xffff0000, v68
	v_and_b32_e32 v2, 0xffff0000, v60
	v_pk_mul_f32 v[34:35], v[34:35], v[46:47]
	v_pk_mov_b32 v[46:47], v[18:19], v[2:3] op_sel:[1,0]
	ds_write_b128 v7, v[98:101]
	v_pk_fma_f32 v[30:31], v[8:9], v[46:47], v[30:31] op_sel_hi:[0,1,1]
	v_and_b32_e32 v7, 0xffff0000, v64
	v_mov_b32_e32 v6, v3
	v_pk_fma_f32 v[30:31], v[12:13], v[2:3], v[30:31] op_sel_hi:[0,1,1]
	v_pk_fma_f32 v[2:3], v[22:23], v[2:3], v[26:27] op_sel_hi:[0,1,0]
	v_and_b32_e32 v11, 0xffff0000, v72
	v_mov_b32_e32 v10, v7
	v_pk_fma_f32 v[2:3], v[8:9], v[6:7], v[2:3] op_sel_hi:[0,1,1]
	v_and_b32_e32 v15, 0xffff0000, v76
	v_mov_b32_e32 v14, v11
	v_pk_fma_f32 v[38:39], v[8:9], v[62:63], v[38:39] op_sel_hi:[0,1,1]
	v_pk_fma_f32 v[2:3], v[12:13], v[10:11], v[2:3] op_sel_hi:[0,1,1]
	v_pk_fma_f32 v[18:19], v[12:13], v[18:19], v[38:39] op_sel_hi:[0,1,1]
	v_pk_fma_f32 v[2:3], v[4:5], v[14:15], v[2:3] op_sel_hi:[0,1,1]
	v_pk_fma_f32 v[18:19], v[4:5], v[46:47], v[18:19] op_sel_hi:[0,1,1]
	v_pk_fma_f32 v[30:31], v[4:5], v[6:7], v[30:31] op_sel_hi:[0,1,1]
	v_mul_f32_e32 v4, 0xbfb8aa3b, v2
	v_exp_f32_e32 v4, v4
	v_mul_f32_e32 v6, 0xbfb8aa3b, v3
	v_exp_f32_e32 v7, v6
	v_mul_f32_e32 v16, 0xbfb8aa3b, v18
	v_add_f32_e32 v4, 1.0, v4
	v_rcp_f32_e32 v6, v4
	v_add_f32_e32 v4, 1.0, v7
	v_rcp_f32_e32 v7, v4
	v_pk_mul_f32 v[42:43], v[42:43], v[54:55]
	v_exp_f32_e32 v16, v16
	v_mul_f32_e32 v20, 0xbfb8aa3b, v19
	v_pk_mul_f32 v[2:3], v[2:3], v[6:7]
	v_cvt_pk_bf16_f32 v99, v58, v59
	v_lshlrev_b32_e32 v54, 16, v5
	v_lshlrev_b32_e32 v55, 16, v17
	v_lshlrev_b32_e32 v58, 16, v9
	v_lshlrev_b32_e32 v59, 16, v13
	v_pk_mul_f32 v[50:51], v[50:51], v[118:119]
	v_exp_f32_e32 v20, v20
	v_pk_mul_f32 v[2:3], v[2:3], v[132:133]
	v_pk_fma_f32 v[62:63], v[92:93], v[58:59], v[96:97] op_sel_hi:[0,1,0]
	v_pk_mov_b32 v[58:59], v[58:59], v[54:55] op_sel:[1,0]
	v_pk_mul_f32 v[66:67], v[66:67], v[120:121]
	v_cvt_pk_bf16_f32 v100, v50, v51
	v_cvt_pk_bf16_f32 v105, v2, v3
	v_add_u32_e32 v2, 5, v134
	v_lshlrev_b32_e32 v51, 16, v25
	v_lshlrev_b32_e32 v50, 16, v21
	v_pk_fma_f32 v[58:59], v[80:81], v[58:59], v[62:63] op_sel_hi:[0,1,1]
	v_cvt_pk_bf16_f32 v98, v66, v67
	v_lshlrev_b32_e32 v4, 2, v2
	v_pk_mov_b32 v[66:67], v[54:55], v[50:51] op_sel:[1,0]
	v_pk_fma_f32 v[58:59], v[84:85], v[54:55], v[58:59] op_sel_hi:[0,1,1]
	v_add_f32_e32 v16, 1.0, v16
	v_lshlrev_b32_e32 v3, 8, v2
	v_and_b32_e32 v4, 12, v4
	v_bfe_u32 v2, v2, 2, 2
	v_pk_fma_f32 v[58:59], v[88:89], v[66:67], v[58:59] op_sel_hi:[0,1,1]
	v_rcp_f32_e32 v38, v16
	v_add_f32_e32 v16, 1.0, v20
	v_bitop3_b32 v6, v4, v136, v2 bitop3:0x36
	v_bitop3_b32 v2, v4, v135, v2 bitop3:0x36
	v_mul_f32_e32 v4, 0xbfb8aa3b, v58
	v_rcp_f32_e32 v39, v16
	v_exp_f32_e32 v4, v4
	v_mul_f32_e32 v8, 0xbfb8aa3b, v59
	v_pk_mul_f32 v[42:43], v[42:43], v[126:127]
	v_exp_f32_e32 v8, v8
	v_pk_fma_f32 v[54:55], v[92:93], v[54:55], v[96:97] op_sel_hi:[0,1,0]
	v_cvt_pk_bf16_f32 v101, v42, v43
	v_lshlrev_b32_e32 v43, 16, v33
	v_lshlrev_b32_e32 v42, 16, v29
	v_pk_fma_f32 v[54:55], v[80:81], v[66:67], v[54:55] op_sel_hi:[0,1,1]
	v_pk_mov_b32 v[70:71], v[50:51], v[42:43] op_sel:[1,0]
	v_pk_fma_f32 v[54:55], v[84:85], v[50:51], v[54:55] op_sel_hi:[0,1,1]
	v_pk_mul_f32 v[18:19], v[18:19], v[38:39]
	v_add_f32_e32 v4, 1.0, v4
	v_pk_fma_f32 v[54:55], v[88:89], v[70:71], v[54:55] op_sel_hi:[0,1,1]
	v_pk_mul_f32 v[10:11], v[18:19], v[122:123]
	v_rcp_f32_e32 v62, v4
	v_add_f32_e32 v4, 1.0, v8
	v_mul_f32_e32 v8, 0xbfb8aa3b, v54
	v_mul_f32_e32 v16, 0xbfb8aa3b, v30
	v_cvt_pk_bf16_f32 v103, v10, v11
	v_exp_f32_e32 v8, v8
	v_mul_f32_e32 v10, 0xbfb8aa3b, v55
	v_rcp_f32_e32 v63, v4
	v_exp_f32_e32 v16, v16
	v_mul_f32_e32 v20, 0xbfb8aa3b, v31
	v_exp_f32_e32 v10, v10
	v_pk_mul_f32 v[34:35], v[34:35], v[128:129]
	v_exp_f32_e32 v20, v20
	v_pk_fma_f32 v[50:51], v[92:93], v[50:51], v[96:97] op_sel_hi:[0,1,0]
	v_cvt_pk_bf16_f32 v102, v34, v35
	v_lshlrev_b32_e32 v35, 16, v41
	v_lshlrev_b32_e32 v34, 16, v37
	v_pk_fma_f32 v[50:51], v[80:81], v[70:71], v[50:51] op_sel_hi:[0,1,1]
	v_pk_fma_f32 v[46:47], v[92:93], v[42:43], v[96:97] op_sel_hi:[0,1,0]
	v_add_f32_e32 v4, 1.0, v8
	v_pk_mul_f32 v[58:59], v[58:59], v[62:63]
	v_pk_mov_b32 v[62:63], v[42:43], v[34:35] op_sel:[1,0]
	v_pk_fma_f32 v[42:43], v[84:85], v[42:43], v[50:51] op_sel_hi:[0,1,1]
	v_add_f32_e32 v16, 1.0, v16
	v_rcp_f32_e32 v66, v4
	v_add_f32_e32 v4, 1.0, v10
	v_pk_fma_f32 v[42:43], v[88:89], v[62:63], v[42:43] op_sel_hi:[0,1,1]
	v_rcp_f32_e32 v38, v16
	v_add_f32_e32 v16, 1.0, v20
	v_rcp_f32_e32 v67, v4
	v_mul_f32_e32 v4, 0xbfb8aa3b, v42
	v_rcp_f32_e32 v39, v16
	v_exp_f32_e32 v4, v4
	v_mul_f32_e32 v8, 0xbfb8aa3b, v43
	v_exp_f32_e32 v8, v8
	v_lshlrev_b32_e32 v27, 16, v49
	v_lshlrev_b32_e32 v26, 16, v45
	v_pk_fma_f32 v[46:47], v[80:81], v[62:63], v[46:47] op_sel_hi:[0,1,1]
	v_pk_mul_f32 v[14:15], v[30:31], v[38:39]
	v_pk_fma_f32 v[38:39], v[92:93], v[34:35], v[96:97] op_sel_hi:[0,1,0]
	v_pk_mul_f32 v[54:55], v[54:55], v[66:67]
	v_add_f32_e32 v4, 1.0, v4
	v_pk_mov_b32 v[66:67], v[34:35], v[26:27] op_sel:[1,0]
	v_pk_fma_f32 v[34:35], v[84:85], v[34:35], v[46:47] op_sel_hi:[0,1,1]
	v_pk_mul_f32 v[50:51], v[54:55], v[124:125]
	v_rcp_f32_e32 v54, v4
	v_add_f32_e32 v4, 1.0, v8
	v_pk_fma_f32 v[34:35], v[88:89], v[66:67], v[34:35] op_sel_hi:[0,1,1]
	v_rcp_f32_e32 v55, v4
	v_mul_f32_e32 v4, 0xbfb8aa3b, v34
	v_exp_f32_e32 v4, v4
	v_mul_f32_e32 v8, 0xbfb8aa3b, v35
	v_exp_f32_e32 v8, v8
	v_lshlrev_b32_e32 v19, 16, v57
	v_lshlrev_b32_e32 v18, 16, v53
	v_pk_fma_f32 v[38:39], v[80:81], v[66:67], v[38:39] op_sel_hi:[0,1,1]
	v_pk_fma_f32 v[30:31], v[92:93], v[26:27], v[96:97] op_sel_hi:[0,1,0]
	v_pk_mul_f32 v[42:43], v[42:43], v[54:55]
	v_pk_mov_b32 v[54:55], v[26:27], v[18:19] op_sel:[1,0]
	v_pk_fma_f32 v[26:27], v[84:85], v[26:27], v[38:39] op_sel_hi:[0,1,1]
	v_add_f32_e32 v4, 1.0, v4
	v_pk_fma_f32 v[26:27], v[88:89], v[54:55], v[26:27] op_sel_hi:[0,1,1]
	v_rcp_f32_e32 v46, v4
	v_add_f32_e32 v4, 1.0, v8
	v_mul_f32_e32 v8, 0xbfb8aa3b, v26
	v_exp_f32_e32 v8, v8
	v_mul_f32_e32 v10, 0xbfb8aa3b, v27
	v_exp_f32_e32 v10, v10
	v_rcp_f32_e32 v47, v4
	v_add_f32_e32 v4, 1.0, v8
	v_rcp_f32_e32 v38, v4
	v_add_f32_e32 v4, 1.0, v10
	v_rcp_f32_e32 v39, v4
	v_pk_mul_f32 v[14:15], v[14:15], v[130:131]
	v_lshlrev_b32_e32 v2, 4, v2
	v_cvt_pk_bf16_f32 v104, v14, v15
	v_lshlrev_b32_e32 v6, 4, v6
	v_add3_u32 v2, v0, v2, v3
	v_add3_u32 v6, v0, v6, v3
	ds_write_b128 v2, v[102:105]
	v_lshlrev_b32_e32 v2, 16, v61
	v_lshlrev_b32_e32 v3, 16, v69
	v_pk_fma_f32 v[30:31], v[80:81], v[54:55], v[30:31] op_sel_hi:[0,1,1]
	v_pk_fma_f32 v[22:23], v[92:93], v[18:19], v[96:97] op_sel_hi:[0,1,0]
	v_pk_mul_f32 v[26:27], v[26:27], v[38:39]
	v_pk_mov_b32 v[38:39], v[18:19], v[2:3] op_sel:[1,0]
	v_pk_fma_f32 v[18:19], v[84:85], v[18:19], v[30:31] op_sel_hi:[0,1,1]
	v_pk_fma_f32 v[18:19], v[88:89], v[38:39], v[18:19] op_sel_hi:[0,1,1]
	v_mul_f32_e32 v4, 0xbfb8aa3b, v18
	v_exp_f32_e32 v4, v4
	v_mul_f32_e32 v8, 0xbfb8aa3b, v19
	v_exp_f32_e32 v8, v8
	v_pk_fma_f32 v[22:23], v[80:81], v[38:39], v[22:23] op_sel_hi:[0,1,1]
	ds_write_b128 v6, v[98:101]
	v_lshlrev_b32_e32 v7, 16, v65
	v_mov_b32_e32 v6, v3
	v_add_f32_e32 v4, 1.0, v4
	v_pk_fma_f32 v[22:23], v[84:85], v[2:3], v[22:23] op_sel_hi:[0,1,1]
	v_pk_fma_f32 v[2:3], v[92:93], v[2:3], v[96:97] op_sel_hi:[0,1,0]
	v_lshlrev_b32_e32 v15, 16, v73
	v_mov_b32_e32 v14, v7
	v_rcp_f32_e32 v30, v4
	v_add_f32_e32 v4, 1.0, v8
	v_pk_fma_f32 v[22:23], v[88:89], v[6:7], v[22:23] op_sel_hi:[0,1,1]
	v_pk_fma_f32 v[2:3], v[80:81], v[6:7], v[2:3] op_sel_hi:[0,1,1]
	v_lshlrev_b32_e32 v11, 16, v77
	v_rcp_f32_e32 v31, v4
	v_mul_f32_e32 v4, 0xbfb8aa3b, v22
	v_mov_b32_e32 v10, v15
	v_pk_fma_f32 v[2:3], v[84:85], v[14:15], v[2:3] op_sel_hi:[0,1,1]
	v_exp_f32_e32 v4, v4
	v_mul_f32_e32 v8, 0xbfb8aa3b, v23
	v_pk_fma_f32 v[2:3], v[88:89], v[10:11], v[2:3] op_sel_hi:[0,1,1]
	v_exp_f32_e32 v8, v8
	v_mul_f32_e32 v6, 0xbfb8aa3b, v2
	v_exp_f32_e32 v6, v6
	v_mul_f32_e32 v7, 0xbfb8aa3b, v3
	v_exp_f32_e32 v7, v7
	v_add_f32_e32 v4, 1.0, v4
	v_pk_mul_f32 v[18:19], v[18:19], v[30:31]
	v_rcp_f32_e32 v30, v4
	v_add_f32_e32 v4, 1.0, v8
	v_rcp_f32_e32 v31, v4
	v_add_f32_e32 v4, 1.0, v6
	v_rcp_f32_e32 v6, v4
	v_add_f32_e32 v4, 1.0, v7
	v_rcp_f32_e32 v7, v4
	v_pk_mul_f32 v[42:43], v[42:43], v[118:119]
	v_mov_b32_e32 v8, v97
	v_and_b32_e32 v17, 0xffff0000, v17
	v_pk_mul_f32 v[2:3], v[2:3], v[6:7]
	v_and_b32_e32 v16, 0xffff0000, v5
	v_pk_mul_f32 v[2:3], v[2:3], v[132:133]
	v_and_b32_e32 v13, 0xffff0000, v13
	v_cvt_pk_bf16_f32 v105, v2, v3
	v_add_u32_e32 v2, 6, v134
	v_lshlrev_b32_e32 v4, 2, v2
	v_lshlrev_b32_e32 v3, 8, v2
	v_and_b32_e32 v4, 12, v4
	v_bfe_u32 v2, v2, 2, 2
	v_bitop3_b32 v6, v4, v136, v2 bitop3:0x36
	v_bitop3_b32 v2, v4, v135, v2 bitop3:0x36
	v_mov_b32_e32 v4, v93
	v_and_b32_e32 v12, 0xffff0000, v9
	v_pk_mul_f32 v[34:35], v[34:35], v[46:47]
	v_cvt_pk_bf16_f32 v100, v42, v43
	v_and_b32_e32 v24, 0xffff0000, v21
	v_pk_fma_f32 v[20:21], v[4:5], v[12:13], v[8:9] op_sel_hi:[0,1,0]
	v_mov_b32_e32 v42, v81
	v_pk_mov_b32 v[12:13], v[12:13], v[16:17] op_sel:[1,0]
	v_pk_mul_f32 v[34:35], v[34:35], v[126:127]
	v_and_b32_e32 v25, 0xffff0000, v25
	v_pk_fma_f32 v[12:13], v[42:43], v[12:13], v[20:21] op_sel_hi:[0,1,1]
	v_mov_b32_e32 v20, v85
	v_pk_mul_f32 v[26:27], v[26:27], v[128:129]
	v_cvt_pk_bf16_f32 v101, v34, v35
	v_and_b32_e32 v35, 0xffff0000, v41
	v_mov_b32_e32 v38, v89
	v_pk_mov_b32 v[40:41], v[16:17], v[24:25] op_sel:[1,0]
	v_pk_fma_f32 v[12:13], v[20:21], v[16:17], v[12:13] op_sel_hi:[0,1,1]
	v_pk_mul_f32 v[10:11], v[18:19], v[122:123]
	v_cvt_pk_bf16_f32 v102, v26, v27
	v_and_b32_e32 v19, 0xffff0000, v57
	v_and_b32_e32 v18, 0xffff0000, v53
	v_and_b32_e32 v27, 0xffff0000, v49
	v_and_b32_e32 v26, 0xffff0000, v45
	v_and_b32_e32 v34, 0xffff0000, v37
	v_and_b32_e32 v33, 0xffff0000, v33
	v_and_b32_e32 v32, 0xffff0000, v29
	v_pk_fma_f32 v[12:13], v[38:39], v[40:41], v[12:13] op_sel_hi:[0,1,1]
	v_pk_mul_f32 v[14:15], v[22:23], v[30:31]
	v_pk_fma_f32 v[22:23], v[4:5], v[18:19], v[8:9] op_sel_hi:[0,1,0]
	v_pk_fma_f32 v[30:31], v[4:5], v[26:27], v[8:9] op_sel_hi:[0,1,0]
	v_pk_fma_f32 v[36:37], v[4:5], v[34:35], v[8:9] op_sel_hi:[0,1,0]
	v_pk_fma_f32 v[28:29], v[4:5], v[32:33], v[8:9] op_sel_hi:[0,1,0]
	v_mul_f32_e32 v5, 0xbfb8aa3b, v12
	v_mul_f32_e32 v9, 0xbfb8aa3b, v13
	v_exp_f32_e32 v5, v5
	v_exp_f32_e32 v9, v9
	v_pk_mov_b32 v[46:47], v[24:25], v[32:33] op_sel:[1,0]
	v_pk_mul_f32 v[14:15], v[14:15], v[130:131]
	v_lshlrev_b32_e32 v2, 4, v2
	v_pk_fma_f32 v[16:17], v[4:5], v[16:17], v[8:9] op_sel_hi:[0,1,0]
	v_pk_fma_f32 v[16:17], v[42:43], v[40:41], v[16:17] op_sel_hi:[0,1,1]
	v_pk_fma_f32 v[16:17], v[20:21], v[24:25], v[16:17] op_sel_hi:[0,1,1]
	v_add_f32_e32 v5, 1.0, v5
	v_pk_fma_f32 v[16:17], v[38:39], v[46:47], v[16:17] op_sel_hi:[0,1,1]
	v_rcp_f32_e32 v44, v5
	v_add_f32_e32 v5, 1.0, v9
	v_mul_f32_e32 v9, 0xbfb8aa3b, v16
	v_exp_f32_e32 v9, v9
	v_mul_f32_e32 v21, 0xbfb8aa3b, v17
	v_exp_f32_e32 v21, v21
	v_rcp_f32_e32 v45, v5
	v_add_f32_e32 v5, 1.0, v9
	v_rcp_f32_e32 v40, v5
	v_add_f32_e32 v5, 1.0, v21
	v_rcp_f32_e32 v41, v5
	v_pk_fma_f32 v[24:25], v[4:5], v[24:25], v[8:9] op_sel_hi:[0,1,0]
	v_pk_fma_f32 v[24:25], v[42:43], v[46:47], v[24:25] op_sel_hi:[0,1,1]
	v_pk_fma_f32 v[24:25], v[20:21], v[32:33], v[24:25] op_sel_hi:[0,1,1]
	v_pk_mul_f32 v[16:17], v[16:17], v[40:41]
	v_pk_mov_b32 v[40:41], v[32:33], v[34:35] op_sel:[1,0]
	v_pk_mul_f32 v[12:13], v[12:13], v[44:45]
	v_pk_fma_f32 v[24:25], v[38:39], v[40:41], v[24:25] op_sel_hi:[0,1,1]
	v_mul_f32_e32 v5, 0xbfb8aa3b, v24
	v_exp_f32_e32 v5, v5
	v_mul_f32_e32 v9, 0xbfb8aa3b, v25
	v_exp_f32_e32 v9, v9
	v_pk_fma_f32 v[28:29], v[42:43], v[40:41], v[28:29] op_sel_hi:[0,1,1]
	v_add_f32_e32 v5, 1.0, v5
	v_pk_mov_b32 v[44:45], v[34:35], v[26:27] op_sel:[1,0]
	v_pk_fma_f32 v[28:29], v[20:21], v[34:35], v[28:29] op_sel_hi:[0,1,1]
	v_rcp_f32_e32 v32, v5
	v_add_f32_e32 v5, 1.0, v9
	v_pk_fma_f32 v[28:29], v[38:39], v[44:45], v[28:29] op_sel_hi:[0,1,1]
	v_rcp_f32_e32 v33, v5
	v_mul_f32_e32 v5, 0xbfb8aa3b, v28
	v_exp_f32_e32 v5, v5
	v_mul_f32_e32 v9, 0xbfb8aa3b, v29
	v_exp_f32_e32 v9, v9
	v_pk_fma_f32 v[36:37], v[42:43], v[44:45], v[36:37] op_sel_hi:[0,1,1]
	v_pk_mov_b32 v[34:35], v[26:27], v[18:19] op_sel:[1,0]
	v_pk_fma_f32 v[26:27], v[20:21], v[26:27], v[36:37] op_sel_hi:[0,1,1]
	v_add_f32_e32 v5, 1.0, v5
	v_pk_fma_f32 v[26:27], v[38:39], v[34:35], v[26:27] op_sel_hi:[0,1,1]
	v_pk_mul_f32 v[24:25], v[24:25], v[32:33]
	v_rcp_f32_e32 v32, v5
	v_add_f32_e32 v5, 1.0, v9
	v_mul_f32_e32 v9, 0xbfb8aa3b, v26
	v_mul_f32_e32 v21, 0xbfb8aa3b, v27
	v_exp_f32_e32 v9, v9
	v_exp_f32_e32 v21, v21
	v_rcp_f32_e32 v33, v5
	v_cvt_pk_bf16_f32 v103, v10, v11
	v_cvt_pk_bf16_f32 v104, v14, v15
	v_lshlrev_b32_e32 v6, 4, v6
	v_add3_u32 v2, v0, v2, v3
	v_add3_u32 v6, v0, v6, v3
	ds_write_b128 v2, v[102:105]
	v_and_b32_e32 v3, 0xffff0000, v69
	v_and_b32_e32 v2, 0xffff0000, v61
	v_pk_fma_f32 v[30:31], v[42:43], v[34:35], v[30:31] op_sel_hi:[0,1,1]
	v_add_f32_e32 v5, 1.0, v9
	v_pk_mul_f32 v[28:29], v[28:29], v[32:33]
	v_pk_mov_b32 v[32:33], v[18:19], v[2:3] op_sel:[1,0]
	v_pk_fma_f32 v[18:19], v[20:21], v[18:19], v[30:31] op_sel_hi:[0,1,1]
	v_rcp_f32_e32 v36, v5
	v_add_f32_e32 v5, 1.0, v21
	v_pk_fma_f32 v[18:19], v[38:39], v[32:33], v[18:19] op_sel_hi:[0,1,1]
	v_rcp_f32_e32 v37, v5
	v_mul_f32_e32 v5, 0xbfb8aa3b, v18
	v_exp_f32_e32 v5, v5
	v_mul_f32_e32 v9, 0xbfb8aa3b, v19
	v_exp_f32_e32 v9, v9
	v_pk_mul_f32 v[58:59], v[58:59], v[120:121]
	v_cvt_pk_bf16_f32 v99, v50, v51
	v_cvt_pk_bf16_f32 v98, v58, v59
	v_pk_fma_f32 v[22:23], v[42:43], v[32:33], v[22:23] op_sel_hi:[0,1,1]
	ds_write_b128 v6, v[98:101]
	v_and_b32_e32 v7, 0xffff0000, v65
	v_mov_b32_e32 v6, v3
	v_add_f32_e32 v5, 1.0, v5
	v_pk_fma_f32 v[22:23], v[20:21], v[2:3], v[22:23] op_sel_hi:[0,1,1]
	v_rcp_f32_e32 v30, v5
	v_add_f32_e32 v5, 1.0, v9
	v_pk_fma_f32 v[22:23], v[38:39], v[6:7], v[22:23] op_sel_hi:[0,1,1]
	v_rcp_f32_e32 v31, v5
	v_mul_f32_e32 v5, 0xbfb8aa3b, v22
	v_exp_f32_e32 v5, v5
	v_mul_f32_e32 v9, 0xbfb8aa3b, v23
	v_exp_f32_e32 v9, v9
	v_pk_mul_f32 v[18:19], v[18:19], v[30:31]
	v_add_f32_e32 v5, 1.0, v5
	v_rcp_f32_e32 v30, v5
	v_add_f32_e32 v5, 1.0, v9
	v_pk_fma_f32 v[2:3], v[4:5], v[2:3], v[8:9] op_sel_hi:[0,1,0]
	v_and_b32_e32 v11, 0xffff0000, v73
	v_mov_b32_e32 v10, v7
	v_pk_fma_f32 v[2:3], v[42:43], v[6:7], v[2:3] op_sel_hi:[0,1,1]
	v_and_b32_e32 v15, 0xffff0000, v77
	v_mov_b32_e32 v14, v11
	v_pk_fma_f32 v[2:3], v[20:21], v[10:11], v[2:3] op_sel_hi:[0,1,1]
	v_pk_fma_f32 v[2:3], v[38:39], v[14:15], v[2:3] op_sel_hi:[0,1,1]
	v_mul_f32_e32 v4, 0xbfb8aa3b, v2
	v_mul_f32_e32 v6, 0xbfb8aa3b, v3
	v_exp_f32_e32 v4, v4
	v_exp_f32_e32 v6, v6
	v_rcp_f32_e32 v31, v5
	v_pk_mul_f32 v[8:9], v[18:19], v[122:123]
	v_add_f32_e32 v4, 1.0, v4
	v_add_f32_e32 v5, 1.0, v6
	v_rcp_f32_e32 v4, v4
	v_rcp_f32_e32 v5, v5
	v_pk_mul_f32 v[6:7], v[22:23], v[30:31]
	v_pk_mul_f32 v[12:13], v[12:13], v[120:121]
	v_pk_mul_f32 v[10:11], v[6:7], v[130:131]
	v_pk_mul_f32 v[2:3], v[2:3], v[4:5]
	v_cvt_pk_bf16_f32 v7, v8, v9
	v_cvt_pk_bf16_f32 v8, v10, v11
	v_add_u32_e32 v10, 7, v134
	v_pk_mul_f32 v[14:15], v[2:3], v[132:133]
	v_cvt_pk_bf16_f32 v2, v12, v13
	v_lshlrev_b32_e32 v12, 2, v10
	v_lshlrev_b32_e32 v11, 8, v10
	v_and_b32_e32 v12, 12, v12
	v_bfe_u32 v10, v10, 2, 2
	v_bitop3_b32 v13, v12, v136, v10 bitop3:0x36
	v_pk_mul_f32 v[16:17], v[16:17], v[124:125]
	v_pk_mul_f32 v[24:25], v[24:25], v[118:119]
	v_pk_mul_f32 v[28:29], v[28:29], v[126:127]
	v_lshlrev_b32_e32 v13, 4, v13
	s_lshl_b64 s[38:39], s[44:45], 9
	s_lshl_b32 s12, s20, 4
	v_readlane_b32 s18, v253, 50
	v_cvt_pk_bf16_f32 v3, v16, v17
	v_cvt_pk_bf16_f32 v4, v24, v25
	v_cvt_pk_bf16_f32 v5, v28, v29
	v_add3_u32 v13, v0, v13, v11
	s_add_u32 s18, s38, s18
	v_pk_mul_f32 v[26:27], v[26:27], v[36:37]
	ds_write_b128 v13, v[2:5]
	v_bitop3_b32 v2, v12, v135, v10 bitop3:0x36
	s_addc_u32 s20, s39, 0
	v_pk_mul_f32 v[26:27], v[26:27], v[128:129]
	v_lshlrev_b32_e32 v2, 4, v2
	s_add_u32 s18, s18, s88
	v_cvt_pk_bf16_f32 v6, v26, v27
	v_cvt_pk_bf16_f32 v9, v14, v15
	v_add3_u32 v0, v0, v2, v11
	v_mov_b32_e32 v87, v184
	s_addc_u32 s21, s20, 0
	ds_write_b128 v0, v[6:9]
	s_waitcnt lgkmcnt(0)
	s_barrier
	s_add_u32 s20, s18, s12
	v_bfe_u32 v127, v87, 2, 2
	v_ashrrev_i32_e32 v6, 2, v87
	v_lshrrev_b32_e32 v7, 3, v87
	v_bfe_u32 v8, v87, 1, 1
	s_addc_u32 s21, s21, 0
	v_and_or_b32 v61, v6, -8, v127
	v_and_or_b32 v83, v7, 2, v8
	v_readlane_b32 s12, v254, 28
	v_lshrrev_b32_e32 v6, 2, v6
	s_lshl_b64 s[20:21], s[20:21], 14
	v_or_b32_e32 v62, s12, v83
	v_lshlrev_b32_e32 v58, 2, v127
	v_and_b32_e32 v59, 2, v6
	s_add_u32 s20, s27, s20
	v_bitop3_b32 v6, v58, v62, v59 bitop3:0x36
	v_lshlrev_b32_e32 v7, 3, v87
	v_ashrrev_i32_e32 v149, 5, v87
	v_and_b32_e32 v86, 31, v87
	s_addc_u32 s21, s85, s21
	v_lshlrev_b32_e32 v6, 4, v6
	s_add_i32 s12, 0, 0x1a000
	v_and_b32_e32 v82, 8, v7
	v_lshlrev_b32_e32 v0, 8, v86
	v_lshlrev_b32_e32 v84, 3, v149
	v_add3_u32 v63, s12, v6, v82
	v_or_b32_e32 v6, 4, v61
	v_lshl_add_u64 v[2:3], s[20:21], 0, v[0:1]
	v_ashrrev_i32_e32 v85, 31, v84
	v_bfe_u32 v60, v6, 2, 2
	v_lshl_add_u64 v[50:51], v[84:85], 1, v[2:3]
	v_lshlrev_b32_e32 v128, 8, v6
	v_bitop3_b32 v6, v60, v62, v58 bitop3:0x36
	s_movk_i32 s18, 0x2000
	v_lshlrev_b32_e32 v88, 8, v61
	v_lshlrev_b32_e32 v6, 4, v6
	v_add_co_u32_e32 v52, vcc, s18, v50
	v_add_u32_e32 v89, v63, v88
	v_add3_u32 v6, s12, v6, v128
	v_addc_co_u32_e32 v53, vcc, 0, v51, vcc
	v_add_co_u32_e32 v182, vcc, 0x2000, v50
	s_nop 1
	v_addc_co_u32_e32 v183, vcc, 0, v51, vcc
	v_add_co_u32_e32 v232, vcc, 0x4000, v50
	s_nop 1
	v_addc_co_u32_e32 v233, vcc, 0, v51, vcc
	v_add_co_u32_e32 v250, vcc, 0x6000, v50
	s_nop 1
	v_addc_co_u32_e32 v251, vcc, 0, v51, vcc
	global_load_dwordx4 v[158:161], v[182:183], off
	global_load_dwordx4 v[162:165], v[50:51], off
	global_load_dwordx4 v[166:169], v[232:233], off
	global_load_dwordx4 v[170:173], v[250:251], off
	global_load_dwordx4 v[174:177], v[50:51], off offset:32
	global_load_dwordx4 v[178:181], v[182:183], off offset:32
	global_load_dwordx4 v[186:189], v[232:233], off offset:32
	global_load_dwordx4 v[190:193], v[250:251], off offset:32
	global_load_dwordx4 v[194:197], v[50:51], off offset:64
	global_load_dwordx4 v[198:201], v[182:183], off offset:64
	global_load_dwordx4 v[202:205], v[232:233], off offset:64
	global_load_dwordx4 v[206:209], v[250:251], off offset:64
	global_load_dwordx4 v[212:215], v[50:51], off offset:96
	global_load_dwordx4 v[216:219], v[182:183], off offset:96
	global_load_dwordx4 v[220:223], v[232:233], off offset:96
	global_load_dwordx4 v[224:227], v[250:251], off offset:96
	global_load_dwordx4 v[240:243], v[50:51], off offset:128
	global_load_dwordx4 v[244:247], v[182:183], off offset:128
	v_add_u32_e32 v90, v6, v82
	ds_read_b64_tr_b16 v[64:65], v89
	ds_read_b64_tr_b16 v[66:67], v90
	s_movk_i32 s18, 0x4000
	v_add_co_u32_e32 v54, vcc, s18, v50
	s_movk_i32 s18, 0x6000
	s_nop 0
	v_addc_co_u32_e32 v55, vcc, 0, v51, vcc
	v_add_co_u32_e32 v56, vcc, s18, v50
	s_waitcnt lgkmcnt(0)
	s_waitcnt vmcnt(17)
	v_mfma_f32_32x32x16_bf16 v[34:49], v[158:161], v[64:67], 0
	global_load_dwordx4 v[158:161], v[232:233], off offset:128
	v_addc_co_u32_e32 v57, vcc, 0, v51, vcc
	v_add_u32_e32 v91, 0x1000, v88
	v_add_u32_e32 v92, v63, v91
	v_add_u32_e32 v94, 0x2000, v88
	s_waitcnt vmcnt(17)
	v_mfma_f32_32x32x16_bf16 v[2:17], v[162:165], v[64:67], 0
	global_load_dwordx4 v[162:165], v[250:251], off offset:128
	v_add_u32_e32 v95, v63, v94
	v_add_u32_e32 v97, 0x3000, v88
	s_add_i32 s18, 0, 0x12000
	v_add_u32_e32 v84, 0, v84
	s_waitcnt vmcnt(17)
	v_mfma_f32_32x32x16_bf16 v[18:33], v[166:169], v[64:67], 0
	global_load_dwordx4 v[166:169], v[50:51], off offset:160
	s_waitcnt vmcnt(17)
	v_mfma_f32_32x32x16_bf16 v[66:81], v[170:173], v[64:67], 0
	global_load_dwordx4 v[170:173], v[182:183], off offset:160
	v_add_u32_e32 v64, 20, v61
	v_bfe_u32 v126, v64, 2, 2
	v_lshlrev_b32_e32 v129, 8, v64
	v_bitop3_b32 v64, v126, v62, v58 bitop3:0x36
	v_lshlrev_b32_e32 v64, 4, v64
	v_add3_u32 v64, s12, v64, v129
	v_add_u32_e32 v93, v64, v82
	ds_read_b64_tr_b16 v[114:115], v92
	ds_read_b64_tr_b16 v[116:117], v93
	v_add_u32_e32 v64, 36, v61
	v_bfe_u32 v131, v64, 2, 2
	v_lshlrev_b32_e32 v130, 8, v64
	v_bitop3_b32 v64, v131, v62, v58 bitop3:0x36
	v_lshlrev_b32_e32 v64, 4, v64
	v_add3_u32 v64, s12, v64, v130
	v_add_u32_e32 v96, v64, v82
	ds_read_b64_tr_b16 v[122:123], v95
	ds_read_b64_tr_b16 v[124:125], v96
	s_waitcnt lgkmcnt(2)
	s_waitcnt vmcnt(17)
	v_mfma_f32_32x32x16_bf16 v[2:17], v[174:177], v[114:117], v[2:17]
	global_load_dwordx4 v[174:177], v[232:233], off offset:160
	v_add_u32_e32 v64, 52, v61
	v_bfe_u32 v145, v64, 2, 2
	v_lshlrev_b32_e32 v144, 8, v64
	v_bitop3_b32 v64, v145, v62, v58 bitop3:0x36
	v_lshlrev_b32_e32 v64, 4, v64
	s_waitcnt vmcnt(17)
	v_mfma_f32_32x32x16_bf16 v[34:49], v[178:181], v[114:117], v[34:49]
	global_load_dwordx4 v[178:181], v[250:251], off offset:160
	v_add3_u32 v64, s12, v64, v144
	s_waitcnt vmcnt(17)
	v_mfma_f32_32x32x16_bf16 v[18:33], v[186:189], v[114:117], v[18:33]
	global_load_dwordx4 v[186:189], v[50:51], off offset:192
	s_waitcnt vmcnt(17)
	v_mfma_f32_32x32x16_bf16 v[66:81], v[190:193], v[114:117], v[66:81]
	global_load_dwordx4 v[190:193], v[182:183], off offset:192
	s_waitcnt lgkmcnt(0)
	s_waitcnt vmcnt(17)
	v_mfma_f32_32x32x16_bf16 v[2:17], v[194:197], v[122:125], v[2:17]
	global_load_dwordx4 v[194:197], v[232:233], off offset:192
	s_waitcnt vmcnt(17)
	v_mfma_f32_32x32x16_bf16 v[34:49], v[198:201], v[122:125], v[34:49]
	global_load_dwordx4 v[198:201], v[250:251], off offset:192
	v_add_u32_e32 v98, v63, v97
	v_add_u32_e32 v99, v64, v82
	v_add_u32_e32 v64, 0x44, v61
	v_bfe_u32 v147, v64, 2, 2
	v_lshlrev_b32_e32 v146, 8, v64
	v_bitop3_b32 v64, v147, v62, v58 bitop3:0x36
	v_add_u32_e32 v100, 0x4000, v88
	s_waitcnt vmcnt(17)
	v_mfma_f32_32x32x16_bf16 v[18:33], v[202:205], v[122:125], v[18:33]
	global_load_dwordx4 v[202:205], v[50:51], off offset:224
	v_lshlrev_b32_e32 v64, 4, v64
	v_add_u32_e32 v101, v63, v100
	v_add3_u32 v64, s12, v64, v146
	v_add_u32_e32 v102, v64, v82
	v_add_u32_e32 v64, 0x54, v61
	v_bfe_u32 v150, v64, 2, 2
	v_lshlrev_b32_e32 v148, 8, v64
	s_waitcnt vmcnt(17)
	v_mfma_f32_32x32x16_bf16 v[66:81], v[206:209], v[122:125], v[66:81]
	global_load_dwordx4 v[206:209], v[182:183], off offset:224
	ds_read_b64_tr_b16 v[104:105], v98
	ds_read_b64_tr_b16 v[106:107], v99
	ds_read_b64_tr_b16 v[122:123], v101
	ds_read_b64_tr_b16 v[124:125], v102
	v_bitop3_b32 v64, v150, v62, v58 bitop3:0x36
	v_add_u32_e32 v103, 0x5000, v88
	v_lshlrev_b32_e32 v64, 4, v64
	v_add3_u32 v64, s12, v64, v148
	s_waitcnt lgkmcnt(2)
	s_waitcnt vmcnt(17)
	v_mfma_f32_32x32x16_bf16 v[2:17], v[212:215], v[104:107], v[2:17]
	global_load_dwordx4 v[212:215], v[232:233], off offset:224
	s_waitcnt vmcnt(17)
	v_mfma_f32_32x32x16_bf16 v[34:49], v[216:219], v[104:107], v[34:49]
	global_load_dwordx4 v[216:219], v[250:251], off offset:224
	s_waitcnt vmcnt(17)
	v_mfma_f32_32x32x16_bf16 v[18:33], v[220:223], v[104:107], v[18:33]
	s_waitcnt vmcnt(16)
	v_mfma_f32_32x32x16_bf16 v[66:81], v[224:227], v[104:107], v[66:81]
	s_waitcnt lgkmcnt(0)
	s_waitcnt vmcnt(15)
	v_mfma_f32_32x32x16_bf16 v[2:17], v[240:243], v[122:125], v[2:17]
	s_waitcnt vmcnt(14)
	v_mfma_f32_32x32x16_bf16 v[34:49], v[244:247], v[122:125], v[34:49]
	s_waitcnt vmcnt(13)
	v_mfma_f32_32x32x16_bf16 v[18:33], v[158:161], v[122:125], v[18:33]
	s_waitcnt vmcnt(12)
	v_mfma_f32_32x32x16_bf16 v[66:81], v[162:165], v[122:125], v[66:81]
	v_add_u32_e32 v104, v63, v103
	v_add_u32_e32 v105, v64, v82
	ds_read_b64_tr_b16 v[122:123], v104
	ds_read_b64_tr_b16 v[124:125], v105
	v_add_u32_e32 v64, 0x64, v61
	v_bfe_u32 v152, v64, 2, 2
	v_lshlrev_b32_e32 v151, 8, v64
	v_bitop3_b32 v64, v152, v62, v58 bitop3:0x36
	v_add_u32_e32 v106, 0x6000, v88
	v_lshlrev_b32_e32 v64, 4, v64
	v_add_u32_e32 v107, v63, v106
	v_add3_u32 v64, s12, v64, v151
	v_add_u32_e32 v108, v64, v82
	ds_read_b64_tr_b16 v[140:141], v107
	ds_read_b64_tr_b16 v[142:143], v108
	s_waitcnt lgkmcnt(2)
	s_waitcnt vmcnt(11)
	v_mfma_f32_32x32x16_bf16 v[2:17], v[166:169], v[122:125], v[2:17]
	v_add_u32_e32 v61, 0x74, v61
	s_waitcnt vmcnt(10)
	v_mfma_f32_32x32x16_bf16 v[34:49], v[170:173], v[122:125], v[34:49]
	s_waitcnt vmcnt(9)
	v_mfma_f32_32x32x16_bf16 v[18:33], v[174:177], v[122:125], v[18:33]
	s_waitcnt vmcnt(8)
	v_mfma_f32_32x32x16_bf16 v[66:81], v[178:181], v[122:125], v[66:81]
	s_nop 0
	s_nop 0
	s_waitcnt lgkmcnt(0)
	s_waitcnt vmcnt(7)
	v_mfma_f32_32x32x16_bf16 v[2:17], v[186:189], v[140:143], v[2:17]
	v_lshlrev_b32_e32 v136, 8, v61
	v_bfe_u32 v61, v61, 2, 2
	v_bitop3_b32 v62, v61, v62, v58 bitop3:0x36
	v_lshlrev_b32_e32 v62, 4, v62
	v_add3_u32 v62, s12, v62, v136
	v_readlane_b32 s12, v254, 25
	s_waitcnt vmcnt(6)
	v_mfma_f32_32x32x16_bf16 v[34:49], v[190:193], v[140:143], v[34:49]
	v_add_u32_e32 v111, 0x7000, v88
	v_add_u32_e32 v113, v63, v111
	v_or_b32_e32 v110, s12, v86
	v_lshl_add_u32 v85, v110, 2, 0
	v_readlane_b32 s12, v253, 46
	v_add_u32_e32 v137, -8, v110
	v_add_u32_e32 v138, -9, v110
	s_waitcnt vmcnt(5)
	v_mfma_f32_32x32x16_bf16 v[18:33], v[194:197], v[140:143], v[18:33]
	v_add_u32_e32 v114, v62, v82
	ds_read_b64_tr_b16 v[62:63], v113
	ds_read_b64_tr_b16 v[64:65], v114
	v_add_u32_e32 v109, s12, v85
	v_readlane_b32 s12, v254, 12
	v_or_b32_e32 v117, v58, v59
	v_add_u32_e32 v139, -10, v110
	v_add_u32_e32 v112, s12, v85
	s_waitcnt vmcnt(4)
	v_mfma_f32_32x32x16_bf16 v[66:81], v[198:201], v[140:143], v[66:81]
	ds_read_b32 v115, v109 offset:2048
	ds_read_b32 v116, v112 offset:2048
	v_or_b32_e32 v119, v126, v58
	v_or_b32_e32 v118, v60, v58
	v_or_b32_e32 v120, v131, v58
	v_or_b32_e32 v121, v145, v58
	s_mov_b32 s12, 0
	v_add_u32_e32 v140, -11, v110
	s_waitcnt lgkmcnt(2)
	s_waitcnt vmcnt(3)
	v_mfma_f32_32x32x16_bf16 v[2:17], v[202:205], v[62:65], v[2:17]
	v_or_b32_e32 v122, v147, v58
	v_or_b32_e32 v123, v150, v58
	v_or_b32_e32 v124, v152, v58
	v_or_b32_e32 v125, v61, v58
	v_add_u32_e32 v141, -16, v110
	v_subrev_u32_e32 v142, 17, v110
	v_subrev_u32_e32 v143, 18, v110
	s_waitcnt vmcnt(2)
	v_mfma_f32_32x32x16_bf16 v[34:49], v[206:209], v[62:65], v[34:49]
	s_waitcnt lgkmcnt(1)
	v_mul_f32_e32 v50, 0x3fb8aa3b, v115
	v_exp_f32_e32 v126, v50
	v_subrev_u32_e32 v145, 24, v110
	v_subrev_u32_e32 v147, 26, v110
	v_pk_mul_f32 v[50:51], v[2:3], v[126:127] op_sel_hi:[1,0]
	s_waitcnt lgkmcnt(0)
	v_mul_f32_e32 v2, 0x3fb8aa3b, v116
	s_waitcnt vmcnt(1)
	v_mfma_f32_32x32x16_bf16 v[18:33], v[212:215], v[62:65], v[18:33]
	v_exp_f32_e32 v2, v2
	v_pk_mul_f32 v[60:61], v[12:13], v[126:127] op_sel_hi:[1,0]
	v_pk_mul_f32 v[58:59], v[10:11], v[126:127] op_sel_hi:[1,0]
	v_pk_mul_f32 v[52:53], v[4:5], v[126:127] op_sel_hi:[1,0]
	v_pk_mul_f32 v[48:49], v[48:49], v[126:127] op_sel_hi:[1,0]
	v_pk_mul_f32 v[46:47], v[46:47], v[126:127] op_sel_hi:[1,0]
	v_pk_mul_f32 v[44:45], v[44:45], v[126:127] op_sel_hi:[1,0]
	s_waitcnt vmcnt(0)
	v_mfma_f32_32x32x16_bf16 v[66:81], v[216:219], v[62:65], v[66:81]
	v_mul_f32_e64 v64, v16, v126
	v_mul_f32_e64 v65, v17, v126
	v_mul_f32_e64 v62, v14, v126
	v_mul_f32_e64 v63, v15, v126
	v_mul_f32_e64 v56, v8, v126
	v_mul_f32_e64 v57, v9, v126
	v_pk_mul_f32 v[54:55], v[6:7], v[126:127] op_sel_hi:[1,0]
	v_pk_mul_f32 v[42:43], v[42:43], v[126:127] op_sel_hi:[1,0]
	v_pk_mul_f32 v[40:41], v[40:41], v[126:127] op_sel_hi:[1,0]
	v_pk_mul_f32 v[38:39], v[38:39], v[126:127] op_sel_hi:[1,0]
	v_pk_mul_f32 v[36:37], v[36:37], v[126:127] op_sel_hi:[1,0]
	v_pk_mul_f32 v[34:35], v[34:35], v[126:127] op_sel_hi:[1,0]
	v_add_u32_e32 v126, s18, v82
	v_readlane_b32 s18, v253, 48
	v_pk_mul_f32 v[32:33], v[32:33], v[2:3] op_sel_hi:[1,0]
	v_pk_mul_f32 v[30:31], v[30:31], v[2:3] op_sel_hi:[1,0]
	v_pk_mul_f32 v[28:29], v[28:29], v[2:3] op_sel_hi:[1,0]
	v_pk_mul_f32 v[26:27], v[26:27], v[2:3] op_sel_hi:[1,0]
	v_pk_mul_f32 v[24:25], v[24:25], v[2:3] op_sel_hi:[1,0]
	v_pk_mul_f32 v[22:23], v[22:23], v[2:3] op_sel_hi:[1,0]
	v_pk_mul_f32 v[20:21], v[20:21], v[2:3] op_sel_hi:[1,0]
	v_pk_mul_f32 v[18:19], v[18:19], v[2:3] op_sel_hi:[1,0]
	v_pk_mul_f32 v[16:17], v[80:81], v[2:3] op_sel_hi:[1,0]
	v_pk_mul_f32 v[14:15], v[78:79], v[2:3] op_sel_hi:[1,0]
	v_pk_mul_f32 v[12:13], v[76:77], v[2:3] op_sel_hi:[1,0]
	v_pk_mul_f32 v[10:11], v[74:75], v[2:3] op_sel_hi:[1,0]
	v_pk_mul_f32 v[8:9], v[72:73], v[2:3] op_sel_hi:[1,0]
	v_pk_mul_f32 v[6:7], v[70:71], v[2:3] op_sel_hi:[1,0]
	v_pk_mul_f32 v[4:5], v[68:69], v[2:3] op_sel_hi:[1,0]
	v_pk_mul_f32 v[2:3], v[66:67], v[2:3] op_sel_hi:[1,0]
	v_lshlrev_b32_e32 v66, 2, v87
	v_add_u32_e32 v135, v126, v136
	v_or_b32_e32 v136, s18, v0
	v_readlane_b32 s18, v253, 49
	v_and_or_b32 v127, v66, 12, v127
	v_lshlrev_b32_e32 v66, 4, v149
	v_or_b32_e32 v0, s18, v0
	v_readlane_b32 s18, v254, 13
	v_lshlrev_b32_e32 v82, 2, v149
	v_add_u32_e32 v128, v126, v128
	v_add_u32_e32 v149, s18, v66
	v_readlane_b32 s18, v254, 14
	v_add_u32_e32 v129, v126, v129
	v_add_u32_e32 v130, v126, v130
	v_add_u32_e32 v131, v126, v144
	v_add_u32_e32 v132, v126, v146
	v_add_u32_e32 v133, v126, v148
	v_add_u32_e32 v134, v126, v151
	v_subrev_u32_e32 v144, 19, v110
	v_subrev_u32_e32 v146, 25, v110
	v_subrev_u32_e32 v148, 27, v110
	v_add_u32_e32 v150, s18, v66
	v_mov_b32_e32 v151, v82
	s_branch .LBB0_588
